# conversion groups 4/2/2 by slot&7; P3 epilogue: all 16 gf gate loads in one batch then multiply+store (was 8 dependent round trips); P8 tail: 7 g chunks fetched in one batch; FoX: removed compiler-ins
# speedup vs baseline: 1.0167x; 1.0096x over previous
.LBB0_202:
	s_bfe_u32 s53, s92, 0x30003
	s_cmpk_gt_u32 s92, 0xbf
	s_cselect_b64 s[0:1], -1, 0
	s_cmpk_eq_i32 s96, 0x100
	s_cselect_b64 s[6:7], -1, 0
	s_and_b64 s[2:3], s[6:7], exec
	s_movk_i32 s2, 0x5800
	v_writelane_b32 v253, s6, 48
	s_cselect_b32 s4, 0x600, 0
	s_cselect_b32 s50, s2, 0x6180
	s_cselect_b32 s95, 0x380, 0
	v_writelane_b32 v253, s7, 49
	s_and_b64 s[6:7], s[0:1], s[6:7]
	s_cmp_gt_u32 s53, 3
	s_mul_i32 s46, s94, s96
	s_cbranch_scc1 .LBB0_563
	s_lshl_b32 s20, s96, 3
	s_abs_i32 s18, s20
	s_waitcnt vmcnt(1)
	v_cvt_f32_u32_e32 v2, s18
	s_sub_i32 s0, 0, s18
	s_add_i32 s14, s20, s50
	s_lshl_b32 s23, s97, 3
	v_rcp_iflag_f32_e32 v2, v2
	s_add_i32 s14, s14, -1
	s_add_i32 s24, s23, s94
	s_abs_i32 s12, s14
	v_mul_f32_e32 v2, 0x4f7ffffe, v2
	v_cvt_u32_f32_e32 v2, v2
	s_nop 0
	v_readfirstlane_b32 s19, v2
	s_mul_i32 s0, s0, s19
	s_mul_hi_u32 s0, s19, s0
	s_add_i32 s19, s19, s0
	s_cmp_ge_i32 s24, s50
	s_mul_hi_u32 s13, s12, s19
	s_cbranch_scc1 .LBB0_211
	s_add_i32 s15, s24, 0xcc0
	s_cmpk_gt_i32 s24, 0xf7ff
	s_cbranch_scc0 .LBB0_212
	s_cmpk_gt_u32 s15, 0x5bf
	s_cbranch_scc0 .LBB0_213
	s_cmpk_gt_u32 s15, 0x6bf
	s_cbranch_scc0 .LBB0_214
	s_cmpk_gt_u32 s15, 0x8bf
	s_cbranch_scc0 .LBB0_215
	s_cmp_lt_u32 s24, 0xfffff340
	s_cbranch_scc0 .LBB0_216
	s_and_b32 s0, s24, 0xffff
	s_mul_i32 s0, s0, 0xaaab
	s_lshr_b32 s10, s0, 24
	s_mul_i32 s11, s10, 0xfffffe80
	s_add_i32 s11, s11, s24
	s_cmpk_gt_i32 s11, 0xff
	s_cbranch_scc0 .LBB0_217
	s_add_i32 s0, s11, 0xffffff00
	s_lshr_b32 s0, s0, 4
	v_readlane_b32 s56, v253, 31
	s_and_b32 s0, s0, 0xffffffe
	s_lshl_b32 s8, s10, 20
	s_lshl_b32 s2, s10, 22
	v_readlane_b32 s66, v253, 41
	v_readlane_b32 s67, v253, 42
	s_add_u32 s2, s66, s2
	s_addc_u32 s3, s67, 0
	s_mov_b32 s1, 0
	s_cmpk_lt_u32 s24, 0x6000
	s_cselect_b32 s9, s3, s85
	s_cselect_b32 s16, s2, s84
	s_lshl_b64 s[2:3], s[0:1], 19
	s_add_u32 s1, s16, s2
	s_addc_u32 s3, s9, s3
	s_lshl_b32 s2, s15, 6
	s_and_b32 s9, s2, 0x7c0
	s_lshl_b32 s2, s9, 2
	s_add_u32 s2, s1, s2
	s_addc_u32 s3, s3, 0
	s_lshl_b32 s1, s9, 9
	s_add_u32 s8, s90, s8
	s_addc_u32 s9, s91, 0
	s_add_u32 s1, s8, s1
	s_addc_u32 s8, s9, 0
	s_lshl_b32 s0, s0, 6
	s_add_u32 s0, s1, s0
	s_addc_u32 s1, s8, 0
	s_add_u32 s0, s0, 0x30c00000
	v_readlane_b32 s57, v253, 32
	v_readlane_b32 s58, v253, 33
	v_readlane_b32 s59, v253, 34
	v_readlane_b32 s60, v253, 35
	v_readlane_b32 s61, v253, 36
	v_readlane_b32 s62, v253, 37
	v_readlane_b32 s63, v253, 38
	v_readlane_b32 s64, v253, 39
	v_readlane_b32 s65, v253, 40
	v_readlane_b32 s68, v253, 43
	v_readlane_b32 s69, v253, 44
	v_readlane_b32 s70, v253, 45
	v_readlane_b32 s71, v253, 46
	s_addc_u32 s1, s1, 0
	s_mov_b64 s[8:9], 0
	s_branch .LBB0_218

.LBB0_699:
	s_cmp_ge_u32 s53, 4
	s_cselect_b32 s36, 1, 0
	s_cmp_ge_u32 s53, 6
	s_cselect_b32 s53, 1, 0
	s_add_i32 s36, s36, s53
	v_readlane_b32 s84, v253, 22
	s_cmp_lg_u32 s36, 1
	v_readlane_b32 s85, v253, 23
	v_readlane_b32 s86, v253, 24
	v_readlane_b32 s87, v253, 25
	v_readlane_b32 s88, v253, 26
	v_readlane_b32 s89, v253, 27
	v_readlane_b32 s90, v253, 28
	v_readlane_b32 s91, v253, 29
	s_cbranch_scc1 .LBB0_1060
	s_lshl_b32 s22, s96, 3
	s_abs_i32 s20, s22
	v_cvt_f32_u32_e32 v2, s20
	s_sub_i32 s0, 0, s20
	s_add_i32 s16, s22, s50
	s_lshl_b32 s25, s97, 3
	v_rcp_iflag_f32_e32 v2, v2
	s_add_i32 s16, s16, -1
	s_add_i32 s26, s25, s94
	s_abs_i32 s14, s16
	v_mul_f32_e32 v2, 0x4f7ffffe, v2
	v_cvt_u32_f32_e32 v2, v2
	s_waitcnt vmcnt(0) lgkmcnt(0)
	s_barrier
	v_readfirstlane_b32 s21, v2
	s_mul_i32 s0, s0, s21
	s_mul_hi_u32 s0, s21, s0
	s_add_i32 s21, s21, s0
	s_cmp_ge_i32 s26, s50
	s_mul_hi_u32 s15, s14, s21
	s_cbranch_scc1 .LBB0_708
	s_add_i32 s17, s26, 0xcc0
	s_cmpk_gt_i32 s26, 0xf7ff
	s_cbranch_scc0 .LBB0_709
	s_cmpk_gt_u32 s17, 0x5bf
	s_cbranch_scc0 .LBB0_710
	s_cmpk_gt_u32 s17, 0x6bf
	s_cbranch_scc0 .LBB0_711
	s_cmpk_gt_u32 s17, 0x8bf
	s_cbranch_scc0 .LBB0_712
	s_cmp_lt_u32 s26, 0xfffff340
	s_cbranch_scc0 .LBB0_713
	s_mul_hi_u32 s0, s26, 0xaaaaaaab
	s_lshr_b32 s10, s0, 8
	s_mul_i32 s18, s10, 0xfffffe80
	s_add_i32 s18, s18, s26
	s_cmpk_gt_i32 s18, 0xff
	s_cbranch_scc0 .LBB0_714
	s_add_i32 s0, s18, 0xffffff00
	s_lshr_b32 s0, s0, 4
	s_lshl_b32 s12, s10, 20
	s_mov_b32 s13, 0
	v_readlane_b32 s56, v253, 31
	s_and_b32 s0, s0, 0xffffffe
	s_lshl_b64 s[2:3], s[12:13], 2
	v_readlane_b32 s66, v253, 41
	v_readlane_b32 s67, v253, 42
	s_add_u32 s1, s66, s2
	s_addc_u32 s2, s67, s3
	s_cmpk_lt_u32 s26, 0x6000
	s_cselect_b32 s12, s1, s84
	s_mov_b32 s1, s13
	s_cselect_b32 s11, s2, s85
	s_lshl_b64 s[2:3], s[0:1], 19
	s_add_u32 s1, s12, s2
	s_addc_u32 s3, s11, s3
	s_lshl_b32 s2, s26, 6
	s_and_b32 s19, s2, 0x7c0
	s_lshl_b32 s2, s19, 2
	s_add_u32 s2, s1, s2
	s_mov_b32 s11, s13
	s_addc_u32 s3, s3, 0
	s_lshl_b64 s[12:13], s[10:11], 20
	s_lshl_b32 s1, s19, 9
	s_add_u32 s11, s90, s12
	s_addc_u32 s12, s91, s13
	s_add_u32 s1, s11, s1
	s_addc_u32 s11, s12, 0
	s_lshl_b32 s0, s0, 6
	s_add_u32 s0, s1, s0
	s_addc_u32 s1, s11, 0
	s_add_u32 s0, s0, 0x30c00000
	v_readlane_b32 s57, v253, 32
	v_readlane_b32 s58, v253, 33
	v_readlane_b32 s59, v253, 34
	v_readlane_b32 s60, v253, 35
	v_readlane_b32 s61, v253, 36
	v_readlane_b32 s62, v253, 37
	v_readlane_b32 s63, v253, 38
	v_readlane_b32 s64, v253, 39
	v_readlane_b32 s65, v253, 40
	v_readlane_b32 s68, v253, 43
	v_readlane_b32 s69, v253, 44
	v_readlane_b32 s70, v253, 45
	v_readlane_b32 s71, v253, 46
	s_addc_u32 s1, s1, 0
	s_mov_b64 s[12:13], 0
	s_branch .LBB0_715

.LBB0_1643:
	v_add_u32_e32 v167, s2, v216
	ds_read_b64_tr_b16 v[162:163], v167 offset:24576
	ds_read_b64_tr_b16 v[164:165], v167 offset:25088
	s_waitcnt lgkmcnt(0)
	v_mfma_f32_32x32x16_bf16 v[50:65], v[158:161], v[110:113], v[50:65]
	v_add_f32_e32 v114, v82, v83
	v_add_f32_e32 v114, v84, v114
	v_add_f32_e32 v114, v85, v114
	v_add_f32_e32 v114, v86, v114
	v_add_f32_e32 v114, v87, v114
	v_cvt_pk_bf16_f32 v126, v82, v83
	v_cvt_pk_bf16_f32 v127, v84, v85
	ds_read_b64_tr_b16 v[82:83], v167 offset:28672
	ds_read_b64_tr_b16 v[84:85], v167 offset:29184
	v_mfma_f32_32x32x16_bf16 v[34:49], v[154:157], v[110:113], v[34:49]
	v_add_f32_e32 v114, v88, v114
	v_add_f32_e32 v114, v89, v114
	v_add_f32_e32 v114, v90, v114
	v_add_f32_e32 v114, v91, v114
	v_cvt_pk_bf16_f32 v128, v86, v87
	v_cvt_pk_bf16_f32 v129, v88, v89
	ds_read_b64_tr_b16 v[86:87], v167 offset:25600
	ds_read_b64_tr_b16 v[88:89], v167 offset:26112
	v_mfma_f32_32x32x16_bf16 v[50:65], v[150:153], v[106:109], v[50:65]
	v_add_f32_e32 v114, v92, v114
	v_add_f32_e32 v114, v93, v114
	v_add_f32_e32 v114, v94, v114
	v_add_f32_e32 v114, v95, v114
	v_cvt_pk_bf16_f32 v122, v90, v91
	v_cvt_pk_bf16_f32 v123, v92, v93
	ds_read_b64_tr_b16 v[90:91], v167 offset:29696
	ds_read_b64_tr_b16 v[92:93], v167 offset:30208
	v_mfma_f32_32x32x16_bf16 v[34:49], v[146:149], v[106:109], v[34:49]
	v_add_f32_e32 v114, v96, v114
	v_add_f32_e32 v114, v97, v114
	v_add_f32_e32 v114, v66, v114
	v_add_f32_e32 v114, v67, v114
	v_cvt_pk_bf16_f32 v124, v94, v95
	v_cvt_pk_bf16_f32 v125, v96, v97
	ds_read_b64_tr_b16 v[94:95], v167 offset:26624
	ds_read_b64_tr_b16 v[96:97], v167 offset:27136
	v_mfma_f32_32x32x16_bf16 v[50:65], v[142:145], v[102:105], v[50:65]
	v_add_f32_e32 v114, v68, v114
	v_add_f32_e32 v114, v69, v114
	v_add_f32_e32 v114, v70, v114
	v_add_f32_e32 v114, v71, v114
	v_cvt_pk_bf16_f32 v118, v66, v67
	v_cvt_pk_bf16_f32 v119, v68, v69
	ds_read_b64_tr_b16 v[66:67], v167 offset:30720
	ds_read_b64_tr_b16 v[68:69], v167 offset:31232
	v_mfma_f32_32x32x16_bf16 v[34:49], v[138:141], v[102:105], v[34:49]
	v_add_f32_e32 v114, v72, v114
	v_add_f32_e32 v114, v73, v114
	v_add_f32_e32 v114, v74, v114
	v_add_f32_e32 v114, v75, v114
	v_cvt_pk_bf16_f32 v120, v70, v71
	v_cvt_pk_bf16_f32 v121, v72, v73
	ds_read_b64_tr_b16 v[70:71], v167 offset:27648
	ds_read_b64_tr_b16 v[72:73], v167 offset:28160
	v_mfma_f32_32x32x16_bf16 v[50:65], v[134:137], v[98:101], v[50:65]
	v_add_f32_e32 v114, v76, v114
	v_add_f32_e32 v114, v77, v114
	v_add_f32_e32 v114, v78, v114
	v_add_f32_e32 v134, v79, v114
	v_cvt_pk_bf16_f32 v114, v74, v75
	v_cvt_pk_bf16_f32 v115, v76, v77
	ds_read_b64_tr_b16 v[74:75], v167 offset:31744
	ds_read_b64_tr_b16 v[76:77], v167 offset:32256
	v_mfma_f32_32x32x16_bf16 v[34:49], v[130:133], v[98:101], v[34:49]
	v_add_f32_e32 v116, v80, v134
	v_add_f32_e32 v116, v81, v116
	v_add_f32_e32 v130, 0, v116
	v_cvt_pk_bf16_f32 v116, v78, v79
	v_cvt_pk_bf16_f32 v117, v80, v81
	v_mfma_f32_32x32x8_bf16 v[50:65], v[196:197], v[200:201], v[50:65]
	v_mfma_f32_32x32x8_bf16 v[34:49], v[196:197], v[200:201], v[34:49]
	v_lshl_add_u64 v[174:175], v[170:171], 0, s[82:83]
	v_lshl_add_u64 v[78:79], v[174:175], 0, s[92:93]
	s_add_i32 m0, s66, s8
	v_lshl_add_u64 v[172:173], v[168:169], 0, s[82:83]
	s_add_i32 s9, s66, s6
	global_load_lds_dwordx4 v[78:79], off
	v_lshl_add_u64 v[78:79], v[172:173], 0, s[72:73]
	s_add_i32 m0, s9, 0x6000
	v_add_f32_e32 v167, v206, v130
	global_load_lds_dwordx4 v[78:79], off
	s_nop 0
	v_max_f32_e32 v78, v51, v51
	v_max_f32_e32 v79, v50, v50
	v_max_f32_e32 v78, v79, v78
	v_max3_f32 v79, v52, v53, v35
	v_max3_f32 v78, v78, v34, v36
	v_max3_f32 v78, v78, v37, v54
	v_max3_f32 v79, v79, v56, v57
	v_max3_f32 v78, v78, v55, v38
	v_max3_f32 v79, v79, v40, v41
	v_max3_f32 v78, v78, v39, v58
	v_max3_f32 v79, v79, v60, v61
	v_max3_f32 v78, v78, v59, v42
	v_max3_f32 v79, v79, v44, v45
	v_max3_f32 v78, v78, v43, v62
	v_max3_f32 v79, v79, v64, v65
	v_max3_f32 v78, v78, v63, v46
	v_max3_f32 v79, v79, v48, v49
	v_max3_f32 v78, v78, v47, v79
	v_mov_b32_e32 v79, v78
	s_nop 1
	v_permlane32_swap_b32 v78, v79
	s_nop 0
	v_max_f32_e32 v79, v79, v79
	v_max_f32_e32 v78, v78, v78
	v_max_f32_e32 v78, v78, v79
	v_cmp_lt_f32_e32 vcc, s95, v78
	s_cmp_lg_u64 vcc, 0
	s_cselect_b64 s[2:3], -1, 0
	s_cbranch_vccnz .LBB0_1651

.LBB0_1646:
	s_add_i32 s2, s6, 0x2000
	s_cmpk_lg_i32 s6, 0x4000
	s_cselect_b32 s97, s2, 0
	v_add_u32_e32 v180, s8, v216
	ds_read_b64_tr_b16 v[134:135], v180 offset:24576
	ds_read_b64_tr_b16 v[136:137], v180 offset:25088
	v_mfma_f32_32x32x16_bf16 v[82:97], v[162:165], v[110:113], v[82:97]
	v_add_f32_e32 v114, v50, v51
	v_add_f32_e32 v114, v52, v114
	v_add_f32_e32 v114, v53, v114
	v_add_f32_e32 v114, v54, v114
	v_add_f32_e32 v114, v55, v114
	v_cvt_pk_bf16_f32 v126, v50, v51
	v_cvt_pk_bf16_f32 v127, v52, v53
	ds_read_b64_tr_b16 v[50:51], v180 offset:28672
	ds_read_b64_tr_b16 v[52:53], v180 offset:29184
	v_mfma_f32_32x32x16_bf16 v[66:81], v[158:161], v[110:113], v[66:81]
	v_add_f32_e32 v114, v56, v114
	v_add_f32_e32 v114, v57, v114
	v_add_f32_e32 v114, v58, v114
	v_add_f32_e32 v114, v59, v114
	v_cvt_pk_bf16_f32 v128, v54, v55
	v_cvt_pk_bf16_f32 v129, v56, v57
	ds_read_b64_tr_b16 v[54:55], v180 offset:25600
	ds_read_b64_tr_b16 v[56:57], v180 offset:26112
	v_mfma_f32_32x32x16_bf16 v[82:97], v[154:157], v[106:109], v[82:97]
	v_add_f32_e32 v114, v60, v114
	v_add_f32_e32 v114, v61, v114
	v_add_f32_e32 v114, v62, v114
	v_add_f32_e32 v114, v63, v114
	v_cvt_pk_bf16_f32 v122, v58, v59
	v_cvt_pk_bf16_f32 v123, v60, v61
	ds_read_b64_tr_b16 v[58:59], v180 offset:29696
	ds_read_b64_tr_b16 v[60:61], v180 offset:30208
	v_mfma_f32_32x32x16_bf16 v[66:81], v[150:153], v[106:109], v[66:81]
	v_add_f32_e32 v114, v64, v114
	v_add_f32_e32 v114, v65, v114
	v_add_f32_e32 v114, v34, v114
	v_add_f32_e32 v114, v35, v114
	v_cvt_pk_bf16_f32 v124, v62, v63
	v_cvt_pk_bf16_f32 v125, v64, v65
	ds_read_b64_tr_b16 v[62:63], v180 offset:26624
	ds_read_b64_tr_b16 v[64:65], v180 offset:27136
	v_mfma_f32_32x32x16_bf16 v[82:97], v[146:149], v[102:105], v[82:97]
	v_add_f32_e32 v114, v36, v114
	v_add_f32_e32 v114, v37, v114
	v_add_f32_e32 v114, v38, v114
	v_add_f32_e32 v114, v39, v114
	v_cvt_pk_bf16_f32 v118, v34, v35
	v_cvt_pk_bf16_f32 v119, v36, v37
	ds_read_b64_tr_b16 v[34:35], v180 offset:30720
	ds_read_b64_tr_b16 v[36:37], v180 offset:31232
	v_mfma_f32_32x32x16_bf16 v[66:81], v[142:145], v[102:105], v[66:81]
	v_add_f32_e32 v114, v40, v114
	v_add_f32_e32 v114, v41, v114
	v_add_f32_e32 v114, v42, v114
	v_add_f32_e32 v114, v43, v114
	v_cvt_pk_bf16_f32 v120, v38, v39
	v_cvt_pk_bf16_f32 v121, v40, v41
	ds_read_b64_tr_b16 v[38:39], v180 offset:27648
	ds_read_b64_tr_b16 v[40:41], v180 offset:28160
	v_mfma_f32_32x32x16_bf16 v[82:97], v[138:141], v[98:101], v[82:97]
	v_add_f32_e32 v114, v44, v114
	v_add_f32_e32 v114, v45, v114
	v_add_f32_e32 v114, v46, v114
	v_add_f32_e32 v138, v47, v114
	v_cvt_pk_bf16_f32 v114, v42, v43
	v_cvt_pk_bf16_f32 v115, v44, v45
	ds_read_b64_tr_b16 v[42:43], v180 offset:31744
	ds_read_b64_tr_b16 v[44:45], v180 offset:32256
	v_mfma_f32_32x32x16_bf16 v[66:81], v[130:133], v[98:101], v[66:81]
	v_add_f32_e32 v116, v48, v138
	v_add_f32_e32 v116, v49, v116
	v_add_f32_e32 v130, 0, v116
	v_cvt_pk_bf16_f32 v116, v46, v47
	v_cvt_pk_bf16_f32 v117, v48, v49
	v_mfma_f32_32x32x8_bf16 v[82:97], v[196:197], v[200:201], v[82:97]
	v_mfma_f32_32x32x8_bf16 v[66:81], v[196:197], v[200:201], v[66:81]
	s_mov_b64 s[2:3], 0x5d51400
	v_lshl_add_u64 v[46:47], v[174:175], 0, s[2:3]
	s_mov_b32 m0, s9
	s_mov_b64 s[2:3], 0x5b31c00
	global_load_lds_dwordx4 v[46:47], off
	v_lshl_add_u64 v[46:47], v[172:173], 0, s[2:3]
	s_add_i32 s2, s66, s97
	s_add_i32 m0, s2, 0x6000
	v_add_f32_e32 v206, v167, v130
	global_load_lds_dwordx4 v[46:47], off
	s_nop 0
	v_max_f32_e32 v46, v83, v83
	v_max_f32_e32 v47, v82, v82
	v_max_f32_e32 v46, v47, v46
	v_max3_f32 v47, v84, v85, v67
	v_max3_f32 v46, v46, v66, v68
	v_max3_f32 v46, v46, v69, v86
	v_max3_f32 v47, v47, v88, v89
	v_max3_f32 v46, v46, v87, v70
	v_max3_f32 v47, v47, v72, v73
	v_max3_f32 v46, v46, v71, v90
	v_max3_f32 v47, v47, v92, v93
	v_max3_f32 v46, v46, v91, v74
	v_max3_f32 v47, v47, v76, v77
	v_max3_f32 v46, v46, v75, v94
	v_max3_f32 v47, v47, v96, v97
	v_max3_f32 v46, v46, v95, v78
	v_max3_f32 v47, v47, v80, v81
	v_max3_f32 v46, v46, v79, v47
	v_mov_b32_e32 v47, v46
	s_nop 1
	v_permlane32_swap_b32 v46, v47
	s_nop 0
	v_max_f32_e32 v47, v47, v47
	v_max_f32_e32 v46, v46, v46
	v_max_f32_e32 v46, v46, v47
	v_cmp_lt_f32_e32 vcc, s95, v46
	s_cmp_lg_u64 vcc, 0
	s_cselect_b64 s[2:3], -1, 0
	s_cbranch_vccnz .LBB0_1654

.LBB0_1663:
	v_add_u32_e32 v166, s6, v216
	ds_read_b64_tr_b16 v[162:163], v166 offset:24576
	ds_read_b64_tr_b16 v[164:165], v166 offset:25088
	s_waitcnt lgkmcnt(0)
	v_mfma_f32_32x32x16_bf16 v[50:65], v[158:161], v[110:113], v[50:65]
	v_add_f32_e32 v114, v82, v83
	v_add_f32_e32 v114, v84, v114
	v_add_f32_e32 v114, v85, v114
	v_add_f32_e32 v114, v86, v114
	v_add_f32_e32 v114, v87, v114
	v_cvt_pk_bf16_f32 v126, v82, v83
	v_cvt_pk_bf16_f32 v127, v84, v85
	ds_read_b64_tr_b16 v[82:83], v166 offset:28672
	ds_read_b64_tr_b16 v[84:85], v166 offset:29184
	v_mfma_f32_32x32x16_bf16 v[34:49], v[154:157], v[110:113], v[34:49]
	v_add_f32_e32 v114, v88, v114
	v_add_f32_e32 v114, v89, v114
	v_add_f32_e32 v114, v90, v114
	v_add_f32_e32 v114, v91, v114
	v_cvt_pk_bf16_f32 v128, v86, v87
	v_cvt_pk_bf16_f32 v129, v88, v89
	ds_read_b64_tr_b16 v[86:87], v166 offset:25600
	ds_read_b64_tr_b16 v[88:89], v166 offset:26112
	v_mfma_f32_32x32x16_bf16 v[50:65], v[150:153], v[106:109], v[50:65]
	v_add_f32_e32 v114, v92, v114
	v_add_f32_e32 v114, v93, v114
	v_add_f32_e32 v114, v94, v114
	v_add_f32_e32 v114, v95, v114
	v_cvt_pk_bf16_f32 v122, v90, v91
	v_cvt_pk_bf16_f32 v123, v92, v93
	ds_read_b64_tr_b16 v[90:91], v166 offset:29696
	ds_read_b64_tr_b16 v[92:93], v166 offset:30208
	v_mfma_f32_32x32x16_bf16 v[34:49], v[146:149], v[106:109], v[34:49]
	v_add_f32_e32 v114, v96, v114
	v_add_f32_e32 v114, v97, v114
	v_add_f32_e32 v114, v66, v114
	v_add_f32_e32 v114, v67, v114
	v_cvt_pk_bf16_f32 v124, v94, v95
	v_cvt_pk_bf16_f32 v125, v96, v97
	ds_read_b64_tr_b16 v[94:95], v166 offset:26624
	ds_read_b64_tr_b16 v[96:97], v166 offset:27136
	v_mfma_f32_32x32x16_bf16 v[50:65], v[142:145], v[102:105], v[50:65]
	v_add_f32_e32 v114, v68, v114
	v_add_f32_e32 v114, v69, v114
	v_add_f32_e32 v114, v70, v114
	v_add_f32_e32 v114, v71, v114
	v_cvt_pk_bf16_f32 v118, v66, v67
	v_cvt_pk_bf16_f32 v119, v68, v69
	ds_read_b64_tr_b16 v[66:67], v166 offset:30720
	ds_read_b64_tr_b16 v[68:69], v166 offset:31232
	v_mfma_f32_32x32x16_bf16 v[34:49], v[138:141], v[102:105], v[34:49]
	v_add_f32_e32 v114, v72, v114
	v_add_f32_e32 v114, v73, v114
	v_add_f32_e32 v114, v74, v114
	v_add_f32_e32 v114, v75, v114
	v_cvt_pk_bf16_f32 v120, v70, v71
	v_cvt_pk_bf16_f32 v121, v72, v73
	ds_read_b64_tr_b16 v[70:71], v166 offset:27648
	ds_read_b64_tr_b16 v[72:73], v166 offset:28160
	v_mfma_f32_32x32x16_bf16 v[50:65], v[134:137], v[98:101], v[50:65]
	v_add_f32_e32 v114, v76, v114
	v_add_f32_e32 v114, v77, v114
	v_add_f32_e32 v114, v78, v114
	v_add_f32_e32 v134, v79, v114
	v_cvt_pk_bf16_f32 v114, v74, v75
	v_cvt_pk_bf16_f32 v115, v76, v77
	ds_read_b64_tr_b16 v[74:75], v166 offset:31744
	ds_read_b64_tr_b16 v[76:77], v166 offset:32256
	v_mfma_f32_32x32x16_bf16 v[34:49], v[130:133], v[98:101], v[34:49]
	v_add_f32_e32 v116, v80, v134
	v_add_f32_e32 v116, v81, v116
	v_add_f32_e32 v130, 0, v116
	v_cvt_pk_bf16_f32 v116, v78, v79
	v_cvt_pk_bf16_f32 v117, v80, v81
	v_mfma_f32_32x32x8_bf16 v[50:65], v[196:197], v[200:201], v[50:65]
	v_mfma_f32_32x32x8_bf16 v[34:49], v[196:197], v[200:201], v[34:49]
	s_add_i32 s2, s84, 1
	s_cmp_ge_u32 s2, s96
	s_cselect_b64 s[88:89], -1, 0
	s_and_b64 vcc, exec, s[88:89]
	v_lshl_add_u64 v[208:209], v[204:205], 0, s[82:83]
	s_cbranch_vccnz .LBB0_1665
	s_mov_b64 s[2:3], 0x5b31400
	v_lshl_add_u64 v[78:79], v[208:209], 0, s[2:3]
	s_add_i32 m0, s66, s97
	s_nop 0
	global_load_lds_dwordx4 v[78:79], off

.LBB0_1674:
	v_add_u32_e32 v164, s97, v216
	ds_read_b64_tr_b16 v[190:191], v164 offset:24576
	ds_read_b64_tr_b16 v[192:193], v164 offset:25088
	v_mfma_f32_32x32x16_bf16 v[82:97], v[158:161], v[110:113], v[82:97]
	v_add_f32_e32 v114, v50, v51
	v_add_f32_e32 v114, v52, v114
	v_add_f32_e32 v114, v53, v114
	v_add_f32_e32 v114, v54, v114
	v_add_f32_e32 v114, v55, v114
	v_cvt_pk_bf16_f32 v126, v50, v51
	v_cvt_pk_bf16_f32 v127, v52, v53
	ds_read_b64_tr_b16 v[186:187], v164 offset:28672
	ds_read_b64_tr_b16 v[188:189], v164 offset:29184
	v_mfma_f32_32x32x16_bf16 v[66:81], v[154:157], v[110:113], v[66:81]
	v_add_f32_e32 v114, v56, v114
	v_add_f32_e32 v114, v57, v114
	v_add_f32_e32 v114, v58, v114
	v_add_f32_e32 v114, v59, v114
	v_cvt_pk_bf16_f32 v128, v54, v55
	v_cvt_pk_bf16_f32 v129, v56, v57
	ds_read_b64_tr_b16 v[182:183], v164 offset:25600
	ds_read_b64_tr_b16 v[184:185], v164 offset:26112
	v_mfma_f32_32x32x16_bf16 v[82:97], v[150:153], v[106:109], v[82:97]
	v_add_f32_e32 v114, v60, v114
	v_add_f32_e32 v114, v61, v114
	v_add_f32_e32 v114, v62, v114
	v_add_f32_e32 v114, v63, v114
	v_cvt_pk_bf16_f32 v122, v58, v59
	v_cvt_pk_bf16_f32 v123, v60, v61
	ds_read_b64_tr_b16 v[178:179], v164 offset:29696
	ds_read_b64_tr_b16 v[180:181], v164 offset:30208
	v_mfma_f32_32x32x16_bf16 v[66:81], v[146:149], v[106:109], v[66:81]
	v_add_f32_e32 v114, v64, v114
	v_add_f32_e32 v114, v65, v114
	v_add_f32_e32 v114, v34, v114
	v_add_f32_e32 v114, v35, v114
	v_cvt_pk_bf16_f32 v124, v62, v63
	v_cvt_pk_bf16_f32 v125, v64, v65
	ds_read_b64_tr_b16 v[174:175], v164 offset:26624
	ds_read_b64_tr_b16 v[176:177], v164 offset:27136
	v_mfma_f32_32x32x16_bf16 v[82:97], v[142:145], v[102:105], v[82:97]
	v_add_f32_e32 v114, v36, v114
	v_add_f32_e32 v114, v37, v114
	v_add_f32_e32 v114, v38, v114
	v_add_f32_e32 v114, v39, v114
	v_cvt_pk_bf16_f32 v118, v34, v35
	v_cvt_pk_bf16_f32 v119, v36, v37
	ds_read_b64_tr_b16 v[170:171], v164 offset:30720
	ds_read_b64_tr_b16 v[172:173], v164 offset:31232
	v_mfma_f32_32x32x16_bf16 v[66:81], v[138:141], v[102:105], v[66:81]
	v_add_f32_e32 v114, v40, v114
	v_add_f32_e32 v114, v41, v114
	v_add_f32_e32 v114, v42, v114
	v_add_f32_e32 v114, v43, v114
	v_cvt_pk_bf16_f32 v120, v38, v39
	v_cvt_pk_bf16_f32 v121, v40, v41
	ds_read_b64_tr_b16 v[166:167], v164 offset:27648
	ds_read_b64_tr_b16 v[168:169], v164 offset:28160
	v_mfma_f32_32x32x16_bf16 v[82:97], v[134:137], v[98:101], v[82:97]
	v_add_f32_e32 v114, v44, v114
	v_add_f32_e32 v114, v45, v114
	v_add_f32_e32 v114, v46, v114
	v_add_f32_e32 v223, v47, v114
	v_cvt_pk_bf16_f32 v114, v42, v43
	v_cvt_pk_bf16_f32 v115, v44, v45
	ds_read_b64_tr_b16 v[162:163], v164 offset:31744
	ds_read_b64_tr_b16 v[164:165], v164 offset:32256
	v_mfma_f32_32x32x16_bf16 v[66:81], v[130:133], v[98:101], v[66:81]
	v_add_f32_e32 v116, v48, v223
	v_add_f32_e32 v116, v49, v116
	v_add_f32_e32 v223, 0, v116
	v_cvt_pk_bf16_f32 v116, v46, v47
	v_cvt_pk_bf16_f32 v117, v48, v49
	v_mfma_f32_32x32x8_bf16 v[82:97], v[196:197], v[200:201], v[82:97]
	v_mfma_f32_32x32x8_bf16 v[66:81], v[196:197], v[200:201], v[66:81]
	s_add_i32 s31, s84, 2
	s_cmp_ge_u32 s31, s96
	s_cselect_b64 s[90:91], -1, 0
	s_and_b64 vcc, exec, s[90:91]
	s_cbranch_vccnz .LBB0_1676
	v_lshl_add_u64 v[208:209], v[208:209], 0, s[92:93]
	s_mov_b32 m0, s74
	s_nop 0
	global_load_lds_dwordx4 v[208:209], off

.LBB0_1711:
	v_add_u32_e32 v166, s30, v216
	ds_read_b64_tr_b16 v[162:163], v166 offset:24576
	ds_read_b64_tr_b16 v[164:165], v166 offset:25088
	s_waitcnt lgkmcnt(0)
	v_mfma_f32_32x32x16_bf16 v[50:65], v[158:161], v[110:113], v[50:65]
	v_add_f32_e32 v114, v82, v83
	v_add_f32_e32 v114, v84, v114
	v_add_f32_e32 v114, v85, v114
	v_add_f32_e32 v114, v86, v114
	v_add_f32_e32 v114, v87, v114
	v_cvt_pk_bf16_f32 v126, v82, v83
	v_cvt_pk_bf16_f32 v127, v84, v85
	ds_read_b64_tr_b16 v[82:83], v166 offset:28672
	ds_read_b64_tr_b16 v[84:85], v166 offset:29184
	v_mfma_f32_32x32x16_bf16 v[34:49], v[154:157], v[110:113], v[34:49]
	v_add_f32_e32 v110, v88, v114
	v_add_f32_e32 v110, v89, v110
	v_add_f32_e32 v110, v90, v110
	v_add_f32_e32 v110, v91, v110
	v_cvt_pk_bf16_f32 v128, v86, v87
	v_cvt_pk_bf16_f32 v129, v88, v89
	ds_read_b64_tr_b16 v[86:87], v166 offset:25600
	ds_read_b64_tr_b16 v[88:89], v166 offset:26112
	v_mfma_f32_32x32x16_bf16 v[50:65], v[150:153], v[106:109], v[50:65]
	v_add_f32_e32 v110, v92, v110
	v_add_f32_e32 v110, v93, v110
	v_add_f32_e32 v110, v94, v110
	v_add_f32_e32 v110, v95, v110
	v_cvt_pk_bf16_f32 v122, v90, v91
	v_cvt_pk_bf16_f32 v123, v92, v93
	ds_read_b64_tr_b16 v[90:91], v166 offset:29696
	ds_read_b64_tr_b16 v[92:93], v166 offset:30208
	v_mfma_f32_32x32x16_bf16 v[34:49], v[146:149], v[106:109], v[34:49]
	v_add_f32_e32 v106, v96, v110
	v_add_f32_e32 v106, v97, v106
	v_add_f32_e32 v106, v66, v106
	v_add_f32_e32 v106, v67, v106
	v_cvt_pk_bf16_f32 v124, v94, v95
	v_cvt_pk_bf16_f32 v125, v96, v97
	ds_read_b64_tr_b16 v[94:95], v166 offset:26624
	ds_read_b64_tr_b16 v[96:97], v166 offset:27136
	v_mfma_f32_32x32x16_bf16 v[50:65], v[142:145], v[102:105], v[50:65]
	v_add_f32_e32 v106, v68, v106
	v_add_f32_e32 v106, v69, v106
	v_add_f32_e32 v106, v70, v106
	v_add_f32_e32 v106, v71, v106
	v_cvt_pk_bf16_f32 v118, v66, v67
	v_cvt_pk_bf16_f32 v119, v68, v69
	ds_read_b64_tr_b16 v[66:67], v166 offset:30720
	ds_read_b64_tr_b16 v[68:69], v166 offset:31232
	v_mfma_f32_32x32x16_bf16 v[34:49], v[138:141], v[102:105], v[34:49]
	v_add_f32_e32 v102, v72, v106
	v_add_f32_e32 v102, v73, v102
	v_add_f32_e32 v102, v74, v102
	v_add_f32_e32 v102, v75, v102
	v_cvt_pk_bf16_f32 v120, v70, v71
	v_cvt_pk_bf16_f32 v121, v72, v73
	ds_read_b64_tr_b16 v[70:71], v166 offset:27648
	ds_read_b64_tr_b16 v[72:73], v166 offset:28160
	v_mfma_f32_32x32x16_bf16 v[50:65], v[134:137], v[98:101], v[50:65]
	v_add_f32_e32 v102, v76, v102
	v_add_f32_e32 v102, v77, v102
	v_add_f32_e32 v102, v78, v102
	v_add_f32_e32 v102, v79, v102
	v_cvt_pk_bf16_f32 v114, v74, v75
	v_cvt_pk_bf16_f32 v115, v76, v77
	ds_read_b64_tr_b16 v[74:75], v166 offset:31744
	ds_read_b64_tr_b16 v[76:77], v166 offset:32256
	v_mfma_f32_32x32x16_bf16 v[34:49], v[130:133], v[98:101], v[34:49]
	v_add_f32_e32 v98, v80, v102
	v_add_f32_e32 v98, v81, v98
	v_add_f32_e32 v98, 0, v98
	v_cvt_pk_bf16_f32 v116, v78, v79
	v_cvt_pk_bf16_f32 v117, v80, v81
	v_mfma_f32_32x32x8_bf16 v[50:65], v[196:197], v[200:201], v[50:65]
	v_mfma_f32_32x32x8_bf16 v[34:49], v[196:197], v[200:201], v[34:49]
	v_add_u32_e32 v79, 0xffffff40, v217
	v_add_f32_e32 v78, v206, v98
	v_cmp_gt_i32_e64 s[62:63], 26, v79
	v_cmp_gt_i32_e64 s[64:65], 27, v79
	v_cmp_gt_i32_e64 s[60:61], 25, v79
	s_and_b64 s[62:63], s[64:65], s[62:63]
	v_cmp_gt_i32_e64 s[58:59], 24, v79
	s_and_b64 s[60:61], s[62:63], s[60:61]
	v_cmp_gt_i32_e64 s[56:57], 19, v79
	s_and_b64 s[58:59], s[60:61], s[58:59]
	v_cmp_gt_i32_e64 s[54:55], 18, v79
	s_and_b64 s[56:57], s[58:59], s[56:57]
	v_cmp_gt_i32_e64 s[52:53], 17, v79
	s_and_b64 s[54:55], s[56:57], s[54:55]
	v_cmp_gt_i32_e64 s[50:51], 16, v79
	s_and_b64 s[52:53], s[54:55], s[52:53]
	v_cmp_gt_i32_e64 s[48:49], 11, v79
	s_and_b64 s[50:51], s[52:53], s[50:51]
	v_cmp_gt_i32_e64 s[46:47], 10, v79
	s_and_b64 s[48:49], s[50:51], s[48:49]
	v_cmp_gt_i32_e64 s[44:45], 9, v79
	s_and_b64 s[46:47], s[48:49], s[46:47]
	v_cmp_gt_i32_e64 s[42:43], 8, v79
	s_and_b64 s[44:45], s[46:47], s[44:45]
	v_cmp_gt_i32_e64 s[40:41], 3, v79
	s_and_b64 s[42:43], s[44:45], s[42:43]
	v_cmp_gt_i32_e64 s[38:39], 2, v79
	s_and_b64 s[40:41], s[42:43], s[40:41]
	v_cmp_gt_i32_e64 s[36:37], 1, v79
	s_and_b64 s[38:39], s[40:41], s[38:39]
	v_cmp_gt_i32_e64 s[34:35], 0, v79
	s_and_b64 s[36:37], s[38:39], s[36:37]
	s_and_b64 s[34:35], s[36:37], s[34:35]
	v_cmp_gt_i32_e64 s[28:29], 58, v79
	v_cndmask_b32_e64 v50, v50, v211, s[34:35]
	v_cmp_gt_i32_e64 s[34:35], 59, v79
	v_cmp_gt_i32_e64 s[26:27], 57, v79
	s_and_b64 s[28:29], s[34:35], s[28:29]
	v_cmp_gt_i32_e64 s[24:25], 56, v79
	s_and_b64 s[26:27], s[28:29], s[26:27]
	v_cmp_gt_i32_e64 s[22:23], 51, v79
	s_and_b64 s[24:25], s[26:27], s[24:25]
	v_cmp_gt_i32_e64 s[20:21], 50, v79
	s_and_b64 s[22:23], s[24:25], s[22:23]
	v_cmp_gt_i32_e64 s[18:19], 49, v79
	s_and_b64 s[20:21], s[22:23], s[20:21]
	v_cmp_gt_i32_e64 s[16:17], 48, v79
	s_and_b64 s[18:19], s[20:21], s[18:19]
	v_cmp_gt_i32_e64 s[14:15], 43, v79
	s_and_b64 s[16:17], s[18:19], s[16:17]
	v_cmp_gt_i32_e64 s[12:13], 42, v79
	s_and_b64 s[14:15], s[16:17], s[14:15]
	v_cmp_gt_i32_e64 s[10:11], 41, v79
	s_and_b64 s[12:13], s[14:15], s[12:13]
	v_cmp_gt_i32_e64 s[8:9], 40, v79
	s_and_b64 s[10:11], s[12:13], s[10:11]
	v_cmp_gt_i32_e64 s[6:7], 35, v79
	s_and_b64 s[8:9], s[10:11], s[8:9]
	v_cmp_gt_i32_e64 s[4:5], 34, v79
	s_and_b64 s[6:7], s[8:9], s[6:7]
	v_cmp_gt_i32_e64 s[2:3], 33, v79
	s_and_b64 s[4:5], s[6:7], s[4:5]
	v_cmp_gt_i32_e32 vcc, 32, v79
	v_cndmask_b32_e64 v51, v51, v211, s[36:37]
	s_and_b64 s[2:3], s[4:5], s[2:3]
	s_and_b64 vcc, s[2:3], vcc
	v_max_f32_e32 v79, v51, v51
	v_max_f32_e32 v80, v50, v50
	v_cndmask_b32_e64 v53, v53, v211, s[40:41]
	v_cndmask_b32_e64 v52, v52, v211, s[38:39]
	v_cndmask_b32_e64 v36, v36, v211, s[4:5]
	v_cndmask_b32_e64 v35, v35, v211, s[2:3]
	v_cndmask_b32_e32 v34, v34, v211, vcc
	v_max_f32_e32 v79, v80, v79
	v_cndmask_b32_e64 v57, v57, v211, s[48:49]
	v_cndmask_b32_e64 v56, v56, v211, s[46:47]
	v_cndmask_b32_e64 v54, v54, v211, s[42:43]
	v_cndmask_b32_e64 v37, v37, v211, s[6:7]
	v_max3_f32 v80, v52, v53, v35
	v_max3_f32 v79, v79, v34, v36
	v_cndmask_b32_e64 v55, v55, v211, s[44:45]
	v_cndmask_b32_e64 v41, v41, v211, s[14:15]
	v_cndmask_b32_e64 v40, v40, v211, s[12:13]
	v_cndmask_b32_e64 v38, v38, v211, s[8:9]
	v_max3_f32 v79, v79, v37, v54
	v_max3_f32 v80, v80, v56, v57
	v_cndmask_b32_e64 v61, v61, v211, s[56:57]
	v_cndmask_b32_e64 v60, v60, v211, s[54:55]
	v_cndmask_b32_e64 v58, v58, v211, s[50:51]
	v_cndmask_b32_e64 v39, v39, v211, s[10:11]
	v_max3_f32 v79, v79, v55, v38
	v_max3_f32 v80, v80, v40, v41
	v_cndmask_b32_e64 v59, v59, v211, s[52:53]
	v_cndmask_b32_e64 v45, v45, v211, s[22:23]
	v_cndmask_b32_e64 v44, v44, v211, s[20:21]
	v_cndmask_b32_e64 v42, v42, v211, s[16:17]
	v_max3_f32 v79, v79, v39, v58
	v_max3_f32 v80, v80, v60, v61
	v_cndmask_b32_e64 v65, v65, v211, s[64:65]
	v_cndmask_b32_e64 v64, v64, v211, s[62:63]
	v_cndmask_b32_e64 v62, v62, v211, s[58:59]
	v_cndmask_b32_e64 v43, v43, v211, s[18:19]
	v_max3_f32 v79, v79, v59, v42
	v_max3_f32 v80, v80, v44, v45
	v_cndmask_b32_e64 v63, v63, v211, s[60:61]
	v_cndmask_b32_e64 v49, v49, v211, s[34:35]
	v_cndmask_b32_e64 v48, v48, v211, s[28:29]
	v_cndmask_b32_e64 v46, v46, v211, s[24:25]
	v_max3_f32 v79, v79, v43, v62
	v_max3_f32 v80, v80, v64, v65
	v_cndmask_b32_e64 v47, v47, v211, s[26:27]
	v_max3_f32 v79, v79, v63, v46
	v_max3_f32 v80, v80, v48, v49
	v_max3_f32 v79, v79, v47, v80
	v_mov_b32_e32 v80, v79
	s_nop 1
	v_permlane32_swap_b32 v79, v80
	s_nop 0
	v_max_f32_e32 v80, v80, v80
	v_max_f32_e32 v79, v79, v79
	v_max_f32_e32 v79, v79, v80
	v_cmp_lt_f32_e32 vcc, s95, v79
	s_cmp_lg_u64 vcc, 0
	s_cselect_b64 s[2:3], -1, 0
	s_cbranch_vccnz .LBB0_1716

.LBB0_1815:
	v_add_u32_e32 v167, s2, v216
	ds_read_b64_tr_b16 v[162:163], v167 offset:24576
	ds_read_b64_tr_b16 v[164:165], v167 offset:25088
	s_waitcnt lgkmcnt(0)
	v_mfma_f32_32x32x16_bf16 v[50:65], v[158:161], v[110:113], v[50:65]
	v_add_f32_e32 v114, v82, v83
	v_add_f32_e32 v114, v84, v114
	v_add_f32_e32 v114, v85, v114
	v_add_f32_e32 v114, v86, v114
	v_add_f32_e32 v114, v87, v114
	v_cvt_pk_bf16_f32 v126, v82, v83
	v_cvt_pk_bf16_f32 v127, v84, v85
	ds_read_b64_tr_b16 v[82:83], v167 offset:28672
	ds_read_b64_tr_b16 v[84:85], v167 offset:29184
	v_mfma_f32_32x32x16_bf16 v[34:49], v[154:157], v[110:113], v[34:49]
	v_add_f32_e32 v114, v88, v114
	v_add_f32_e32 v114, v89, v114
	v_add_f32_e32 v114, v90, v114
	v_add_f32_e32 v114, v91, v114
	v_cvt_pk_bf16_f32 v128, v86, v87
	v_cvt_pk_bf16_f32 v129, v88, v89
	ds_read_b64_tr_b16 v[86:87], v167 offset:25600
	ds_read_b64_tr_b16 v[88:89], v167 offset:26112
	v_mfma_f32_32x32x16_bf16 v[50:65], v[150:153], v[106:109], v[50:65]
	v_add_f32_e32 v114, v92, v114
	v_add_f32_e32 v114, v93, v114
	v_add_f32_e32 v114, v94, v114
	v_add_f32_e32 v114, v95, v114
	v_cvt_pk_bf16_f32 v122, v90, v91
	v_cvt_pk_bf16_f32 v123, v92, v93
	ds_read_b64_tr_b16 v[90:91], v167 offset:29696
	ds_read_b64_tr_b16 v[92:93], v167 offset:30208
	v_mfma_f32_32x32x16_bf16 v[34:49], v[146:149], v[106:109], v[34:49]
	v_add_f32_e32 v114, v96, v114
	v_add_f32_e32 v114, v97, v114
	v_add_f32_e32 v114, v66, v114
	v_add_f32_e32 v114, v67, v114
	v_cvt_pk_bf16_f32 v124, v94, v95
	v_cvt_pk_bf16_f32 v125, v96, v97
	ds_read_b64_tr_b16 v[94:95], v167 offset:26624
	ds_read_b64_tr_b16 v[96:97], v167 offset:27136
	v_mfma_f32_32x32x16_bf16 v[50:65], v[142:145], v[102:105], v[50:65]
	v_add_f32_e32 v114, v68, v114
	v_add_f32_e32 v114, v69, v114
	v_add_f32_e32 v114, v70, v114
	v_add_f32_e32 v114, v71, v114
	v_cvt_pk_bf16_f32 v118, v66, v67
	v_cvt_pk_bf16_f32 v119, v68, v69
	ds_read_b64_tr_b16 v[66:67], v167 offset:30720
	ds_read_b64_tr_b16 v[68:69], v167 offset:31232
	v_mfma_f32_32x32x16_bf16 v[34:49], v[138:141], v[102:105], v[34:49]
	v_add_f32_e32 v114, v72, v114
	v_add_f32_e32 v114, v73, v114
	v_add_f32_e32 v114, v74, v114
	v_add_f32_e32 v114, v75, v114
	v_cvt_pk_bf16_f32 v120, v70, v71
	v_cvt_pk_bf16_f32 v121, v72, v73
	ds_read_b64_tr_b16 v[70:71], v167 offset:27648
	ds_read_b64_tr_b16 v[72:73], v167 offset:28160
	v_mfma_f32_32x32x16_bf16 v[50:65], v[134:137], v[98:101], v[50:65]
	v_add_f32_e32 v114, v76, v114
	v_add_f32_e32 v114, v77, v114
	v_add_f32_e32 v114, v78, v114
	v_add_f32_e32 v134, v79, v114
	v_cvt_pk_bf16_f32 v114, v74, v75
	v_cvt_pk_bf16_f32 v115, v76, v77
	ds_read_b64_tr_b16 v[74:75], v167 offset:31744
	ds_read_b64_tr_b16 v[76:77], v167 offset:32256
	v_mfma_f32_32x32x16_bf16 v[34:49], v[130:133], v[98:101], v[34:49]
	v_add_f32_e32 v116, v80, v134
	v_add_f32_e32 v116, v81, v116
	v_add_f32_e32 v130, 0, v116
	v_cvt_pk_bf16_f32 v116, v78, v79
	v_cvt_pk_bf16_f32 v117, v80, v81
	v_mfma_f32_32x32x8_bf16 v[50:65], v[196:197], v[200:201], v[50:65]
	v_mfma_f32_32x32x8_bf16 v[34:49], v[196:197], v[200:201], v[34:49]
	v_lshl_add_u64 v[174:175], v[170:171], 0, s[70:71]
	v_lshl_add_u64 v[78:79], v[174:175], 0, s[74:75]
	s_add_i32 m0, s82, s8
	v_lshl_add_u64 v[172:173], v[168:169], 0, s[70:71]
	s_add_i32 s9, s82, s6
	global_load_lds_dwordx4 v[78:79], off
	v_lshl_add_u64 v[78:79], v[172:173], 0, s[78:79]
	s_add_i32 m0, s9, 0x6000
	v_add_f32_e32 v167, v206, v130
	global_load_lds_dwordx4 v[78:79], off
	s_nop 0
	v_max_f32_e32 v78, v51, v51
	v_max_f32_e32 v79, v50, v50
	v_max_f32_e32 v78, v79, v78
	v_max3_f32 v79, v52, v53, v35
	v_max3_f32 v78, v78, v34, v36
	v_max3_f32 v78, v78, v37, v54
	v_max3_f32 v79, v79, v56, v57
	v_max3_f32 v78, v78, v55, v38
	v_max3_f32 v79, v79, v40, v41
	v_max3_f32 v78, v78, v39, v58
	v_max3_f32 v79, v79, v60, v61
	v_max3_f32 v78, v78, v59, v42
	v_max3_f32 v79, v79, v44, v45
	v_max3_f32 v78, v78, v43, v62
	v_max3_f32 v79, v79, v64, v65
	v_max3_f32 v78, v78, v63, v46
	v_max3_f32 v79, v79, v48, v49
	v_max3_f32 v78, v78, v47, v79
	v_mov_b32_e32 v79, v78
	s_nop 1
	v_permlane32_swap_b32 v78, v79
	s_nop 0
	v_max_f32_e32 v79, v79, v79
	v_max_f32_e32 v78, v78, v78
	v_max_f32_e32 v78, v78, v79
	v_cmp_lt_f32_e32 vcc, s85, v78
	s_cmp_lg_u64 vcc, 0
	s_cselect_b64 s[2:3], -1, 0
	s_cbranch_vccnz .LBB0_1823

.LBB0_1818:
	s_add_i32 s2, s6, 0x2000
	s_cmpk_lg_i32 s6, 0x4000
	s_cselect_b32 s93, s2, 0
	v_add_u32_e32 v180, s8, v216
	ds_read_b64_tr_b16 v[134:135], v180 offset:24576
	ds_read_b64_tr_b16 v[136:137], v180 offset:25088
	v_mfma_f32_32x32x16_bf16 v[82:97], v[162:165], v[110:113], v[82:97]
	v_add_f32_e32 v114, v50, v51
	v_add_f32_e32 v114, v52, v114
	v_add_f32_e32 v114, v53, v114
	v_add_f32_e32 v114, v54, v114
	v_add_f32_e32 v114, v55, v114
	v_cvt_pk_bf16_f32 v126, v50, v51
	v_cvt_pk_bf16_f32 v127, v52, v53
	ds_read_b64_tr_b16 v[50:51], v180 offset:28672
	ds_read_b64_tr_b16 v[52:53], v180 offset:29184
	v_mfma_f32_32x32x16_bf16 v[66:81], v[158:161], v[110:113], v[66:81]
	v_add_f32_e32 v114, v56, v114
	v_add_f32_e32 v114, v57, v114
	v_add_f32_e32 v114, v58, v114
	v_add_f32_e32 v114, v59, v114
	v_cvt_pk_bf16_f32 v128, v54, v55
	v_cvt_pk_bf16_f32 v129, v56, v57
	ds_read_b64_tr_b16 v[54:55], v180 offset:25600
	ds_read_b64_tr_b16 v[56:57], v180 offset:26112
	v_mfma_f32_32x32x16_bf16 v[82:97], v[154:157], v[106:109], v[82:97]
	v_add_f32_e32 v114, v60, v114
	v_add_f32_e32 v114, v61, v114
	v_add_f32_e32 v114, v62, v114
	v_add_f32_e32 v114, v63, v114
	v_cvt_pk_bf16_f32 v122, v58, v59
	v_cvt_pk_bf16_f32 v123, v60, v61
	ds_read_b64_tr_b16 v[58:59], v180 offset:29696
	ds_read_b64_tr_b16 v[60:61], v180 offset:30208
	v_mfma_f32_32x32x16_bf16 v[66:81], v[150:153], v[106:109], v[66:81]
	v_add_f32_e32 v114, v64, v114
	v_add_f32_e32 v114, v65, v114
	v_add_f32_e32 v114, v34, v114
	v_add_f32_e32 v114, v35, v114
	v_cvt_pk_bf16_f32 v124, v62, v63
	v_cvt_pk_bf16_f32 v125, v64, v65
	ds_read_b64_tr_b16 v[62:63], v180 offset:26624
	ds_read_b64_tr_b16 v[64:65], v180 offset:27136
	v_mfma_f32_32x32x16_bf16 v[82:97], v[146:149], v[102:105], v[82:97]
	v_add_f32_e32 v114, v36, v114
	v_add_f32_e32 v114, v37, v114
	v_add_f32_e32 v114, v38, v114
	v_add_f32_e32 v114, v39, v114
	v_cvt_pk_bf16_f32 v118, v34, v35
	v_cvt_pk_bf16_f32 v119, v36, v37
	ds_read_b64_tr_b16 v[34:35], v180 offset:30720
	ds_read_b64_tr_b16 v[36:37], v180 offset:31232
	v_mfma_f32_32x32x16_bf16 v[66:81], v[142:145], v[102:105], v[66:81]
	v_add_f32_e32 v114, v40, v114
	v_add_f32_e32 v114, v41, v114
	v_add_f32_e32 v114, v42, v114
	v_add_f32_e32 v114, v43, v114
	v_cvt_pk_bf16_f32 v120, v38, v39
	v_cvt_pk_bf16_f32 v121, v40, v41
	ds_read_b64_tr_b16 v[38:39], v180 offset:27648
	ds_read_b64_tr_b16 v[40:41], v180 offset:28160
	v_mfma_f32_32x32x16_bf16 v[82:97], v[138:141], v[98:101], v[82:97]
	v_add_f32_e32 v114, v44, v114
	v_add_f32_e32 v114, v45, v114
	v_add_f32_e32 v114, v46, v114
	v_add_f32_e32 v138, v47, v114
	v_cvt_pk_bf16_f32 v114, v42, v43
	v_cvt_pk_bf16_f32 v115, v44, v45
	ds_read_b64_tr_b16 v[42:43], v180 offset:31744
	ds_read_b64_tr_b16 v[44:45], v180 offset:32256
	v_mfma_f32_32x32x16_bf16 v[66:81], v[130:133], v[98:101], v[66:81]
	v_add_f32_e32 v116, v48, v138
	v_add_f32_e32 v116, v49, v116
	v_add_f32_e32 v130, 0, v116
	v_cvt_pk_bf16_f32 v116, v46, v47
	v_cvt_pk_bf16_f32 v117, v48, v49
	v_mfma_f32_32x32x8_bf16 v[82:97], v[196:197], v[200:201], v[82:97]
	v_mfma_f32_32x32x8_bf16 v[66:81], v[196:197], v[200:201], v[66:81]
	s_mov_b64 s[2:3], 0x5d51400
	v_lshl_add_u64 v[46:47], v[174:175], 0, s[2:3]
	s_mov_b32 m0, s9
	s_mov_b64 s[2:3], 0x5b31c00
	global_load_lds_dwordx4 v[46:47], off
	v_lshl_add_u64 v[46:47], v[172:173], 0, s[2:3]
	s_add_i32 s2, s82, s93
	s_add_i32 m0, s2, 0x6000
	v_add_f32_e32 v206, v167, v130
	global_load_lds_dwordx4 v[46:47], off
	s_nop 0
	v_max_f32_e32 v46, v83, v83
	v_max_f32_e32 v47, v82, v82
	v_max_f32_e32 v46, v47, v46
	v_max3_f32 v47, v84, v85, v67
	v_max3_f32 v46, v46, v66, v68
	v_max3_f32 v46, v46, v69, v86
	v_max3_f32 v47, v47, v88, v89
	v_max3_f32 v46, v46, v87, v70
	v_max3_f32 v47, v47, v72, v73
	v_max3_f32 v46, v46, v71, v90
	v_max3_f32 v47, v47, v92, v93
	v_max3_f32 v46, v46, v91, v74
	v_max3_f32 v47, v47, v76, v77
	v_max3_f32 v46, v46, v75, v94
	v_max3_f32 v47, v47, v96, v97
	v_max3_f32 v46, v46, v95, v78
	v_max3_f32 v47, v47, v80, v81
	v_max3_f32 v46, v46, v79, v47
	v_mov_b32_e32 v47, v46
	s_nop 1
	v_permlane32_swap_b32 v46, v47
	s_nop 0
	v_max_f32_e32 v47, v47, v47
	v_max_f32_e32 v46, v46, v46
	v_max_f32_e32 v46, v46, v47
	v_cmp_lt_f32_e32 vcc, s85, v46
	s_cmp_lg_u64 vcc, 0
	s_cselect_b64 s[2:3], -1, 0
	s_cbranch_vccnz .LBB0_1826

.LBB0_1835:
	v_add_u32_e32 v166, s6, v216
	ds_read_b64_tr_b16 v[162:163], v166 offset:24576
	ds_read_b64_tr_b16 v[164:165], v166 offset:25088
	s_waitcnt lgkmcnt(0)
	v_mfma_f32_32x32x16_bf16 v[50:65], v[158:161], v[110:113], v[50:65]
	v_add_f32_e32 v114, v82, v83
	v_add_f32_e32 v114, v84, v114
	v_add_f32_e32 v114, v85, v114
	v_add_f32_e32 v114, v86, v114
	v_add_f32_e32 v114, v87, v114
	v_cvt_pk_bf16_f32 v126, v82, v83
	v_cvt_pk_bf16_f32 v127, v84, v85
	ds_read_b64_tr_b16 v[82:83], v166 offset:28672
	ds_read_b64_tr_b16 v[84:85], v166 offset:29184
	v_mfma_f32_32x32x16_bf16 v[34:49], v[154:157], v[110:113], v[34:49]
	v_add_f32_e32 v114, v88, v114
	v_add_f32_e32 v114, v89, v114
	v_add_f32_e32 v114, v90, v114
	v_add_f32_e32 v114, v91, v114
	v_cvt_pk_bf16_f32 v128, v86, v87
	v_cvt_pk_bf16_f32 v129, v88, v89
	ds_read_b64_tr_b16 v[86:87], v166 offset:25600
	ds_read_b64_tr_b16 v[88:89], v166 offset:26112
	v_mfma_f32_32x32x16_bf16 v[50:65], v[150:153], v[106:109], v[50:65]
	v_add_f32_e32 v114, v92, v114
	v_add_f32_e32 v114, v93, v114
	v_add_f32_e32 v114, v94, v114
	v_add_f32_e32 v114, v95, v114
	v_cvt_pk_bf16_f32 v122, v90, v91
	v_cvt_pk_bf16_f32 v123, v92, v93
	ds_read_b64_tr_b16 v[90:91], v166 offset:29696
	ds_read_b64_tr_b16 v[92:93], v166 offset:30208
	v_mfma_f32_32x32x16_bf16 v[34:49], v[146:149], v[106:109], v[34:49]
	v_add_f32_e32 v114, v96, v114
	v_add_f32_e32 v114, v97, v114
	v_add_f32_e32 v114, v66, v114
	v_add_f32_e32 v114, v67, v114
	v_cvt_pk_bf16_f32 v124, v94, v95
	v_cvt_pk_bf16_f32 v125, v96, v97
	ds_read_b64_tr_b16 v[94:95], v166 offset:26624
	ds_read_b64_tr_b16 v[96:97], v166 offset:27136
	v_mfma_f32_32x32x16_bf16 v[50:65], v[142:145], v[102:105], v[50:65]
	v_add_f32_e32 v114, v68, v114
	v_add_f32_e32 v114, v69, v114
	v_add_f32_e32 v114, v70, v114
	v_add_f32_e32 v114, v71, v114
	v_cvt_pk_bf16_f32 v118, v66, v67
	v_cvt_pk_bf16_f32 v119, v68, v69
	ds_read_b64_tr_b16 v[66:67], v166 offset:30720
	ds_read_b64_tr_b16 v[68:69], v166 offset:31232
	v_mfma_f32_32x32x16_bf16 v[34:49], v[138:141], v[102:105], v[34:49]
	v_add_f32_e32 v114, v72, v114
	v_add_f32_e32 v114, v73, v114
	v_add_f32_e32 v114, v74, v114
	v_add_f32_e32 v114, v75, v114
	v_cvt_pk_bf16_f32 v120, v70, v71
	v_cvt_pk_bf16_f32 v121, v72, v73
	ds_read_b64_tr_b16 v[70:71], v166 offset:27648
	ds_read_b64_tr_b16 v[72:73], v166 offset:28160
	v_mfma_f32_32x32x16_bf16 v[50:65], v[134:137], v[98:101], v[50:65]
	v_add_f32_e32 v114, v76, v114
	v_add_f32_e32 v114, v77, v114
	v_add_f32_e32 v114, v78, v114
	v_add_f32_e32 v134, v79, v114
	v_cvt_pk_bf16_f32 v114, v74, v75
	v_cvt_pk_bf16_f32 v115, v76, v77
	ds_read_b64_tr_b16 v[74:75], v166 offset:31744
	ds_read_b64_tr_b16 v[76:77], v166 offset:32256
	v_mfma_f32_32x32x16_bf16 v[34:49], v[130:133], v[98:101], v[34:49]
	v_add_f32_e32 v116, v80, v134
	v_add_f32_e32 v116, v81, v116
	v_add_f32_e32 v130, 0, v116
	v_cvt_pk_bf16_f32 v116, v78, v79
	v_cvt_pk_bf16_f32 v117, v80, v81
	v_mfma_f32_32x32x8_bf16 v[50:65], v[196:197], v[200:201], v[50:65]
	v_mfma_f32_32x32x8_bf16 v[34:49], v[196:197], v[200:201], v[34:49]
	s_add_i32 s2, s96, 1
	s_cmp_ge_u32 s2, s92
	s_cselect_b64 s[88:89], -1, 0
	s_and_b64 vcc, exec, s[88:89]
	v_lshl_add_u64 v[208:209], v[204:205], 0, s[70:71]
	s_cbranch_vccnz .LBB0_1837
	s_mov_b64 s[2:3], 0x5b31400
	v_lshl_add_u64 v[78:79], v[208:209], 0, s[2:3]
	s_add_i32 m0, s82, s93
	s_nop 0
	global_load_lds_dwordx4 v[78:79], off

.LBB0_1846:
	v_add_u32_e32 v164, s93, v216
	ds_read_b64_tr_b16 v[190:191], v164 offset:24576
	ds_read_b64_tr_b16 v[192:193], v164 offset:25088
	v_mfma_f32_32x32x16_bf16 v[82:97], v[158:161], v[110:113], v[82:97]
	v_add_f32_e32 v114, v50, v51
	v_add_f32_e32 v114, v52, v114
	v_add_f32_e32 v114, v53, v114
	v_add_f32_e32 v114, v54, v114
	v_add_f32_e32 v114, v55, v114
	v_cvt_pk_bf16_f32 v126, v50, v51
	v_cvt_pk_bf16_f32 v127, v52, v53
	ds_read_b64_tr_b16 v[186:187], v164 offset:28672
	ds_read_b64_tr_b16 v[188:189], v164 offset:29184
	v_mfma_f32_32x32x16_bf16 v[66:81], v[154:157], v[110:113], v[66:81]
	v_add_f32_e32 v114, v56, v114
	v_add_f32_e32 v114, v57, v114
	v_add_f32_e32 v114, v58, v114
	v_add_f32_e32 v114, v59, v114
	v_cvt_pk_bf16_f32 v128, v54, v55
	v_cvt_pk_bf16_f32 v129, v56, v57
	ds_read_b64_tr_b16 v[182:183], v164 offset:25600
	ds_read_b64_tr_b16 v[184:185], v164 offset:26112
	v_mfma_f32_32x32x16_bf16 v[82:97], v[150:153], v[106:109], v[82:97]
	v_add_f32_e32 v114, v60, v114
	v_add_f32_e32 v114, v61, v114
	v_add_f32_e32 v114, v62, v114
	v_add_f32_e32 v114, v63, v114
	v_cvt_pk_bf16_f32 v122, v58, v59
	v_cvt_pk_bf16_f32 v123, v60, v61
	ds_read_b64_tr_b16 v[178:179], v164 offset:29696
	ds_read_b64_tr_b16 v[180:181], v164 offset:30208
	v_mfma_f32_32x32x16_bf16 v[66:81], v[146:149], v[106:109], v[66:81]
	v_add_f32_e32 v114, v64, v114
	v_add_f32_e32 v114, v65, v114
	v_add_f32_e32 v114, v34, v114
	v_add_f32_e32 v114, v35, v114
	v_cvt_pk_bf16_f32 v124, v62, v63
	v_cvt_pk_bf16_f32 v125, v64, v65
	ds_read_b64_tr_b16 v[174:175], v164 offset:26624
	ds_read_b64_tr_b16 v[176:177], v164 offset:27136
	v_mfma_f32_32x32x16_bf16 v[82:97], v[142:145], v[102:105], v[82:97]
	v_add_f32_e32 v114, v36, v114
	v_add_f32_e32 v114, v37, v114
	v_add_f32_e32 v114, v38, v114
	v_add_f32_e32 v114, v39, v114
	v_cvt_pk_bf16_f32 v118, v34, v35
	v_cvt_pk_bf16_f32 v119, v36, v37
	ds_read_b64_tr_b16 v[170:171], v164 offset:30720
	ds_read_b64_tr_b16 v[172:173], v164 offset:31232
	v_mfma_f32_32x32x16_bf16 v[66:81], v[138:141], v[102:105], v[66:81]
	v_add_f32_e32 v114, v40, v114
	v_add_f32_e32 v114, v41, v114
	v_add_f32_e32 v114, v42, v114
	v_add_f32_e32 v114, v43, v114
	v_cvt_pk_bf16_f32 v120, v38, v39
	v_cvt_pk_bf16_f32 v121, v40, v41
	ds_read_b64_tr_b16 v[166:167], v164 offset:27648
	ds_read_b64_tr_b16 v[168:169], v164 offset:28160
	v_mfma_f32_32x32x16_bf16 v[82:97], v[134:137], v[98:101], v[82:97]
	v_add_f32_e32 v114, v44, v114
	v_add_f32_e32 v114, v45, v114
	v_add_f32_e32 v114, v46, v114
	v_add_f32_e32 v223, v47, v114
	v_cvt_pk_bf16_f32 v114, v42, v43
	v_cvt_pk_bf16_f32 v115, v44, v45
	ds_read_b64_tr_b16 v[162:163], v164 offset:31744
	ds_read_b64_tr_b16 v[164:165], v164 offset:32256
	v_mfma_f32_32x32x16_bf16 v[66:81], v[130:133], v[98:101], v[66:81]
	v_add_f32_e32 v116, v48, v223
	v_add_f32_e32 v116, v49, v116
	v_add_f32_e32 v223, 0, v116
	v_cvt_pk_bf16_f32 v116, v46, v47
	v_cvt_pk_bf16_f32 v117, v48, v49
	v_mfma_f32_32x32x8_bf16 v[82:97], v[196:197], v[200:201], v[82:97]
	v_mfma_f32_32x32x8_bf16 v[66:81], v[196:197], v[200:201], v[66:81]
	s_add_i32 s95, s96, 2
	s_cmp_ge_u32 s95, s92
	s_cselect_b64 s[90:91], -1, 0
	s_and_b64 vcc, exec, s[90:91]
	s_cbranch_vccnz .LBB0_1848
	v_lshl_add_u64 v[208:209], v[208:209], 0, s[74:75]
	s_mov_b32 m0, s68
	s_nop 0
	global_load_lds_dwordx4 v[208:209], off

.LBB0_1883:
	v_add_u32_e32 v166, s94, v216
	ds_read_b64_tr_b16 v[162:163], v166 offset:24576
	ds_read_b64_tr_b16 v[164:165], v166 offset:25088
	s_waitcnt lgkmcnt(0)
	v_mfma_f32_32x32x16_bf16 v[50:65], v[158:161], v[110:113], v[50:65]
	v_add_f32_e32 v114, v82, v83
	v_add_f32_e32 v114, v84, v114
	v_add_f32_e32 v114, v85, v114
	v_add_f32_e32 v114, v86, v114
	v_add_f32_e32 v114, v87, v114
	v_cvt_pk_bf16_f32 v126, v82, v83
	v_cvt_pk_bf16_f32 v127, v84, v85
	ds_read_b64_tr_b16 v[82:83], v166 offset:28672
	ds_read_b64_tr_b16 v[84:85], v166 offset:29184
	v_mfma_f32_32x32x16_bf16 v[34:49], v[154:157], v[110:113], v[34:49]
	v_add_f32_e32 v110, v88, v114
	v_add_f32_e32 v110, v89, v110
	v_add_f32_e32 v110, v90, v110
	v_add_f32_e32 v110, v91, v110
	v_cvt_pk_bf16_f32 v128, v86, v87
	v_cvt_pk_bf16_f32 v129, v88, v89
	ds_read_b64_tr_b16 v[86:87], v166 offset:25600
	ds_read_b64_tr_b16 v[88:89], v166 offset:26112
	v_mfma_f32_32x32x16_bf16 v[50:65], v[150:153], v[106:109], v[50:65]
	v_add_f32_e32 v110, v92, v110
	v_add_f32_e32 v110, v93, v110
	v_add_f32_e32 v110, v94, v110
	v_add_f32_e32 v110, v95, v110
	v_cvt_pk_bf16_f32 v122, v90, v91
	v_cvt_pk_bf16_f32 v123, v92, v93
	ds_read_b64_tr_b16 v[90:91], v166 offset:29696
	ds_read_b64_tr_b16 v[92:93], v166 offset:30208
	v_mfma_f32_32x32x16_bf16 v[34:49], v[146:149], v[106:109], v[34:49]
	v_add_f32_e32 v106, v96, v110
	v_add_f32_e32 v106, v97, v106
	v_add_f32_e32 v106, v66, v106
	v_add_f32_e32 v106, v67, v106
	v_cvt_pk_bf16_f32 v124, v94, v95
	v_cvt_pk_bf16_f32 v125, v96, v97
	ds_read_b64_tr_b16 v[94:95], v166 offset:26624
	ds_read_b64_tr_b16 v[96:97], v166 offset:27136
	v_mfma_f32_32x32x16_bf16 v[50:65], v[142:145], v[102:105], v[50:65]
	v_add_f32_e32 v106, v68, v106
	v_add_f32_e32 v106, v69, v106
	v_add_f32_e32 v106, v70, v106
	v_add_f32_e32 v106, v71, v106
	v_cvt_pk_bf16_f32 v118, v66, v67
	v_cvt_pk_bf16_f32 v119, v68, v69
	ds_read_b64_tr_b16 v[66:67], v166 offset:30720
	ds_read_b64_tr_b16 v[68:69], v166 offset:31232
	v_mfma_f32_32x32x16_bf16 v[34:49], v[138:141], v[102:105], v[34:49]
	v_add_f32_e32 v102, v72, v106
	v_add_f32_e32 v102, v73, v102
	v_add_f32_e32 v102, v74, v102
	v_add_f32_e32 v102, v75, v102
	v_cvt_pk_bf16_f32 v120, v70, v71
	v_cvt_pk_bf16_f32 v121, v72, v73
	ds_read_b64_tr_b16 v[70:71], v166 offset:27648
	ds_read_b64_tr_b16 v[72:73], v166 offset:28160
	v_mfma_f32_32x32x16_bf16 v[50:65], v[134:137], v[98:101], v[50:65]
	v_add_f32_e32 v102, v76, v102
	v_add_f32_e32 v102, v77, v102
	v_add_f32_e32 v102, v78, v102
	v_add_f32_e32 v102, v79, v102
	v_cvt_pk_bf16_f32 v114, v74, v75
	v_cvt_pk_bf16_f32 v115, v76, v77
	ds_read_b64_tr_b16 v[74:75], v166 offset:31744
	ds_read_b64_tr_b16 v[76:77], v166 offset:32256
	v_mfma_f32_32x32x16_bf16 v[34:49], v[130:133], v[98:101], v[34:49]
	v_add_f32_e32 v98, v80, v102
	v_add_f32_e32 v98, v81, v98
	v_add_f32_e32 v98, 0, v98
	v_cvt_pk_bf16_f32 v116, v78, v79
	v_cvt_pk_bf16_f32 v117, v80, v81
	v_mfma_f32_32x32x8_bf16 v[50:65], v[196:197], v[200:201], v[50:65]
	v_mfma_f32_32x32x8_bf16 v[34:49], v[196:197], v[200:201], v[34:49]
	v_add_u32_e32 v79, 0xffffff40, v217
	v_add_f32_e32 v78, v206, v98
	v_cmp_gt_i32_e64 s[62:63], 26, v79
	v_cmp_gt_i32_e64 s[64:65], 27, v79
	v_cmp_gt_i32_e64 s[60:61], 25, v79
	s_and_b64 s[62:63], s[64:65], s[62:63]
	v_cmp_gt_i32_e64 s[58:59], 24, v79
	s_and_b64 s[60:61], s[62:63], s[60:61]
	v_cmp_gt_i32_e64 s[56:57], 19, v79
	s_and_b64 s[58:59], s[60:61], s[58:59]
	v_cmp_gt_i32_e64 s[54:55], 18, v79
	s_and_b64 s[56:57], s[58:59], s[56:57]
	v_cmp_gt_i32_e64 s[52:53], 17, v79
	s_and_b64 s[54:55], s[56:57], s[54:55]
	v_cmp_gt_i32_e64 s[50:51], 16, v79
	s_and_b64 s[52:53], s[54:55], s[52:53]
	v_cmp_gt_i32_e64 s[48:49], 11, v79
	s_and_b64 s[50:51], s[52:53], s[50:51]
	v_cmp_gt_i32_e64 s[46:47], 10, v79
	s_and_b64 s[48:49], s[50:51], s[48:49]
	v_cmp_gt_i32_e64 s[44:45], 9, v79
	s_and_b64 s[46:47], s[48:49], s[46:47]
	v_cmp_gt_i32_e64 s[42:43], 8, v79
	s_and_b64 s[44:45], s[46:47], s[44:45]
	v_cmp_gt_i32_e64 s[40:41], 3, v79
	s_and_b64 s[42:43], s[44:45], s[42:43]
	v_cmp_gt_i32_e64 s[38:39], 2, v79
	s_and_b64 s[40:41], s[42:43], s[40:41]
	v_cmp_gt_i32_e64 s[36:37], 1, v79
	s_and_b64 s[38:39], s[40:41], s[38:39]
	v_cmp_gt_i32_e64 s[34:35], 0, v79
	s_and_b64 s[36:37], s[38:39], s[36:37]
	s_and_b64 s[34:35], s[36:37], s[34:35]
	v_cmp_gt_i32_e64 s[28:29], 58, v79
	v_cndmask_b32_e64 v50, v50, v211, s[34:35]
	v_cmp_gt_i32_e64 s[34:35], 59, v79
	v_cmp_gt_i32_e64 s[26:27], 57, v79
	s_and_b64 s[28:29], s[34:35], s[28:29]
	v_cmp_gt_i32_e64 s[24:25], 56, v79
	s_and_b64 s[26:27], s[28:29], s[26:27]
	v_cmp_gt_i32_e64 s[22:23], 51, v79
	s_and_b64 s[24:25], s[26:27], s[24:25]
	v_cmp_gt_i32_e64 s[20:21], 50, v79
	s_and_b64 s[22:23], s[24:25], s[22:23]
	v_cmp_gt_i32_e64 s[18:19], 49, v79
	s_and_b64 s[20:21], s[22:23], s[20:21]
	v_cmp_gt_i32_e64 s[16:17], 48, v79
	s_and_b64 s[18:19], s[20:21], s[18:19]
	v_cmp_gt_i32_e64 s[14:15], 43, v79
	s_and_b64 s[16:17], s[18:19], s[16:17]
	v_cmp_gt_i32_e64 s[12:13], 42, v79
	s_and_b64 s[14:15], s[16:17], s[14:15]
	v_cmp_gt_i32_e64 s[10:11], 41, v79
	s_and_b64 s[12:13], s[14:15], s[12:13]
	v_cmp_gt_i32_e64 s[8:9], 40, v79
	s_and_b64 s[10:11], s[12:13], s[10:11]
	v_cmp_gt_i32_e64 s[6:7], 35, v79
	s_and_b64 s[8:9], s[10:11], s[8:9]
	v_cmp_gt_i32_e64 s[4:5], 34, v79
	s_and_b64 s[6:7], s[8:9], s[6:7]
	v_cmp_gt_i32_e64 s[2:3], 33, v79
	s_and_b64 s[4:5], s[6:7], s[4:5]
	v_cmp_gt_i32_e32 vcc, 32, v79
	v_cndmask_b32_e64 v51, v51, v211, s[36:37]
	s_and_b64 s[2:3], s[4:5], s[2:3]
	s_and_b64 vcc, s[2:3], vcc
	v_max_f32_e32 v79, v51, v51
	v_max_f32_e32 v80, v50, v50
	v_cndmask_b32_e64 v53, v53, v211, s[40:41]
	v_cndmask_b32_e64 v52, v52, v211, s[38:39]
	v_cndmask_b32_e64 v36, v36, v211, s[4:5]
	v_cndmask_b32_e64 v35, v35, v211, s[2:3]
	v_cndmask_b32_e32 v34, v34, v211, vcc
	v_max_f32_e32 v79, v80, v79
	v_cndmask_b32_e64 v57, v57, v211, s[48:49]
	v_cndmask_b32_e64 v56, v56, v211, s[46:47]
	v_cndmask_b32_e64 v54, v54, v211, s[42:43]
	v_cndmask_b32_e64 v37, v37, v211, s[6:7]
	v_max3_f32 v80, v52, v53, v35
	v_max3_f32 v79, v79, v34, v36
	v_cndmask_b32_e64 v55, v55, v211, s[44:45]
	v_cndmask_b32_e64 v41, v41, v211, s[14:15]
	v_cndmask_b32_e64 v40, v40, v211, s[12:13]
	v_cndmask_b32_e64 v38, v38, v211, s[8:9]
	v_max3_f32 v79, v79, v37, v54
	v_max3_f32 v80, v80, v56, v57
	v_cndmask_b32_e64 v61, v61, v211, s[56:57]
	v_cndmask_b32_e64 v60, v60, v211, s[54:55]
	v_cndmask_b32_e64 v58, v58, v211, s[50:51]
	v_cndmask_b32_e64 v39, v39, v211, s[10:11]
	v_max3_f32 v79, v79, v55, v38
	v_max3_f32 v80, v80, v40, v41
	v_cndmask_b32_e64 v59, v59, v211, s[52:53]
	v_cndmask_b32_e64 v45, v45, v211, s[22:23]
	v_cndmask_b32_e64 v44, v44, v211, s[20:21]
	v_cndmask_b32_e64 v42, v42, v211, s[16:17]
	v_max3_f32 v79, v79, v39, v58
	v_max3_f32 v80, v80, v60, v61
	v_cndmask_b32_e64 v65, v65, v211, s[64:65]
	v_cndmask_b32_e64 v64, v64, v211, s[62:63]
	v_cndmask_b32_e64 v62, v62, v211, s[58:59]
	v_cndmask_b32_e64 v43, v43, v211, s[18:19]
	v_max3_f32 v79, v79, v59, v42
	v_max3_f32 v80, v80, v44, v45
	v_cndmask_b32_e64 v63, v63, v211, s[60:61]
	v_cndmask_b32_e64 v49, v49, v211, s[34:35]
	v_cndmask_b32_e64 v48, v48, v211, s[28:29]
	v_cndmask_b32_e64 v46, v46, v211, s[24:25]
	v_max3_f32 v79, v79, v43, v62
	v_max3_f32 v80, v80, v64, v65
	v_cndmask_b32_e64 v47, v47, v211, s[26:27]
	v_max3_f32 v79, v79, v63, v46
	v_max3_f32 v80, v80, v48, v49
	v_max3_f32 v79, v79, v47, v80
	v_mov_b32_e32 v80, v79
	s_nop 1
	v_permlane32_swap_b32 v79, v80
	s_nop 0
	v_max_f32_e32 v80, v80, v80
	v_max_f32_e32 v79, v79, v79
	v_max_f32_e32 v79, v79, v80
	v_cmp_lt_f32_e32 vcc, s85, v79
	s_cmp_lg_u64 vcc, 0
	s_cselect_b64 s[2:3], -1, 0
	s_cbranch_vccnz .LBB0_1888

.LBB0_1940:
	v_mov_b64_e32 v[166:167], s[8:9]
	v_lshlrev_b64 v[130:131], 1, v[164:165]
	v_mad_i64_i32 v[172:173], vcc, v162, s57, v[166:167]
	v_ashrrev_i32_e32 v163, 31, v162
	s_mov_b64 s[26:27], 0x3400
	v_lshl_add_u64 v[172:173], v[172:173], 0, v[130:131]
	v_lshlrev_b64 v[178:179], 12, v[162:163]
	v_lshl_add_u64 v[172:173], v[172:173], 0, s[26:27]
	v_lshl_add_u64 v[178:179], s[10:11], 0, v[178:179]
	s_mov_b64 s[26:27], 0x44000
	v_lshl_add_u64 v[178:179], v[178:179], 0, v[130:131]
	global_load_dwordx4 v[180:183], v[172:173], off
	global_load_dwordx4 v[184:187], v[172:173], off offset:256
	v_lshl_add_u64 v[172:173], v[172:173], 0, s[26:27]
	global_load_dwordx4 v[188:191], v[172:173], off
	global_load_dwordx4 v[192:195], v[172:173], off offset:256
	v_lshl_add_u64 v[172:173], v[172:173], 0, s[26:27]
	global_load_dwordx4 v[200:203], v[172:173], off
	global_load_dwordx4 v[204:207], v[172:173], off offset:256
	v_lshl_add_u64 v[172:173], v[172:173], 0, s[26:27]
	global_load_dwordx4 v[208:211], v[172:173], off
	global_load_dwordx4 v[212:215], v[172:173], off offset:256
	s_mov_b64 s[26:27], 0x154000
	v_lshl_add_u64 v[172:173], v[172:173], 0, s[26:27]
	s_mov_b64 s[26:27], 0x44000
	global_load_dwordx4 v[216:219], v[172:173], off
	global_load_dwordx4 v[220:223], v[172:173], off offset:256
	v_lshl_add_u64 v[172:173], v[172:173], 0, s[26:27]
	global_load_dwordx4 v[224:227], v[172:173], off
	global_load_dwordx4 v[132:135], v[172:173], off offset:256
	v_lshl_add_u64 v[172:173], v[172:173], 0, s[26:27]
	global_load_dwordx4 v[136:139], v[172:173], off
	global_load_dwordx4 v[140:143], v[172:173], off offset:256
	v_lshl_add_u64 v[172:173], v[172:173], 0, s[26:27]
	global_load_dwordx4 v[168:171], v[172:173], off
	global_load_dwordx4 v[164:167], v[172:173], off offset:256
	s_mov_b64 s[26:27], 0x10000
	s_waitcnt vmcnt(15)
	v_lshlrev_b32_e32 v196, 16, v180
	v_and_b32_e32 v197, 0xffff0000, v180
	v_lshlrev_b32_e32 v228, 16, v181
	v_and_b32_e32 v229, 0xffff0000, v181
	v_lshlrev_b32_e32 v180, 16, v182
	v_and_b32_e32 v181, 0xffff0000, v182
	v_lshlrev_b32_e32 v182, 16, v183
	v_and_b32_e32 v183, 0xffff0000, v183
	v_pk_mul_f32 v[126:127], v[126:127], v[196:197]
	v_pk_mul_f32 v[128:129], v[128:129], v[228:229]
	v_pk_mul_f32 v[122:123], v[122:123], v[180:181]
	v_pk_mul_f32 v[124:125], v[124:125], v[182:183]
	v_cvt_pk_bf16_f32 v180, v126, v127
	v_cvt_pk_bf16_f32 v181, v128, v129
	v_cvt_pk_bf16_f32 v182, v122, v123
	v_cvt_pk_bf16_f32 v183, v124, v125
	global_store_dwordx4 v[178:179], v[180:183], off
	s_waitcnt vmcnt(15)
	v_lshlrev_b32_e32 v196, 16, v184
	v_and_b32_e32 v197, 0xffff0000, v184
	v_lshlrev_b32_e32 v228, 16, v185
	v_and_b32_e32 v229, 0xffff0000, v185
	v_lshlrev_b32_e32 v184, 16, v186
	v_and_b32_e32 v185, 0xffff0000, v186
	v_lshlrev_b32_e32 v186, 16, v187
	v_and_b32_e32 v187, 0xffff0000, v187
	v_pk_mul_f32 v[118:119], v[118:119], v[196:197]
	v_pk_mul_f32 v[120:121], v[120:121], v[228:229]
	v_pk_mul_f32 v[114:115], v[114:115], v[184:185]
	v_pk_mul_f32 v[116:117], v[116:117], v[186:187]
	v_cvt_pk_bf16_f32 v184, v118, v119
	v_cvt_pk_bf16_f32 v185, v120, v121
	v_cvt_pk_bf16_f32 v186, v114, v115
	v_cvt_pk_bf16_f32 v187, v116, v117
	global_store_dwordx4 v[178:179], v[184:187], off offset:256
	v_lshl_add_u64 v[178:179], v[178:179], 0, s[26:27]
	s_waitcnt vmcnt(15)
	v_lshlrev_b32_e32 v196, 16, v188
	v_and_b32_e32 v197, 0xffff0000, v188
	v_lshlrev_b32_e32 v228, 16, v189
	v_and_b32_e32 v229, 0xffff0000, v189
	v_lshlrev_b32_e32 v188, 16, v190
	v_and_b32_e32 v189, 0xffff0000, v190
	v_lshlrev_b32_e32 v190, 16, v191
	v_and_b32_e32 v191, 0xffff0000, v191
	v_pk_mul_f32 v[110:111], v[110:111], v[196:197]
	v_pk_mul_f32 v[112:113], v[112:113], v[228:229]
	v_pk_mul_f32 v[106:107], v[106:107], v[188:189]
	v_pk_mul_f32 v[108:109], v[108:109], v[190:191]
	v_cvt_pk_bf16_f32 v188, v110, v111
	v_cvt_pk_bf16_f32 v189, v112, v113
	v_cvt_pk_bf16_f32 v190, v106, v107
	v_cvt_pk_bf16_f32 v191, v108, v109
	global_store_dwordx4 v[178:179], v[188:191], off
	s_waitcnt vmcnt(15)
	v_lshlrev_b32_e32 v196, 16, v192
	v_and_b32_e32 v197, 0xffff0000, v192
	v_lshlrev_b32_e32 v228, 16, v193
	v_and_b32_e32 v229, 0xffff0000, v193
	v_lshlrev_b32_e32 v192, 16, v194
	v_and_b32_e32 v193, 0xffff0000, v194
	v_lshlrev_b32_e32 v194, 16, v195
	v_and_b32_e32 v195, 0xffff0000, v195
	v_pk_mul_f32 v[102:103], v[102:103], v[196:197]
	v_pk_mul_f32 v[104:105], v[104:105], v[228:229]
	v_pk_mul_f32 v[98:99], v[98:99], v[192:193]
	v_pk_mul_f32 v[100:101], v[100:101], v[194:195]
	v_cvt_pk_bf16_f32 v192, v102, v103
	v_cvt_pk_bf16_f32 v193, v104, v105
	v_cvt_pk_bf16_f32 v194, v98, v99
	v_cvt_pk_bf16_f32 v195, v100, v101
	global_store_dwordx4 v[178:179], v[192:195], off offset:256
	v_lshl_add_u64 v[178:179], v[178:179], 0, s[26:27]
	s_waitcnt vmcnt(15)
	v_lshlrev_b32_e32 v196, 16, v200
	v_and_b32_e32 v197, 0xffff0000, v200
	v_lshlrev_b32_e32 v228, 16, v201
	v_and_b32_e32 v229, 0xffff0000, v201
	v_lshlrev_b32_e32 v200, 16, v202
	v_and_b32_e32 v201, 0xffff0000, v202
	v_lshlrev_b32_e32 v202, 16, v203
	v_and_b32_e32 v203, 0xffff0000, v203
	v_pk_mul_f32 v[94:95], v[94:95], v[196:197]
	v_pk_mul_f32 v[96:97], v[96:97], v[228:229]
	v_pk_mul_f32 v[90:91], v[90:91], v[200:201]
	v_pk_mul_f32 v[92:93], v[92:93], v[202:203]
	v_cvt_pk_bf16_f32 v200, v94, v95
	v_cvt_pk_bf16_f32 v201, v96, v97
	v_cvt_pk_bf16_f32 v202, v90, v91
	v_cvt_pk_bf16_f32 v203, v92, v93
	global_store_dwordx4 v[178:179], v[200:203], off
	s_waitcnt vmcnt(15)
	v_lshlrev_b32_e32 v196, 16, v204
	v_and_b32_e32 v197, 0xffff0000, v204
	v_lshlrev_b32_e32 v228, 16, v205
	v_and_b32_e32 v229, 0xffff0000, v205
	v_lshlrev_b32_e32 v204, 16, v206
	v_and_b32_e32 v205, 0xffff0000, v206
	v_lshlrev_b32_e32 v206, 16, v207
	v_and_b32_e32 v207, 0xffff0000, v207
	v_pk_mul_f32 v[86:87], v[86:87], v[196:197]
	v_pk_mul_f32 v[88:89], v[88:89], v[228:229]
	v_pk_mul_f32 v[82:83], v[82:83], v[204:205]
	v_pk_mul_f32 v[84:85], v[84:85], v[206:207]
	v_cvt_pk_bf16_f32 v204, v86, v87
	v_cvt_pk_bf16_f32 v205, v88, v89
	v_cvt_pk_bf16_f32 v206, v82, v83
	v_cvt_pk_bf16_f32 v207, v84, v85
	global_store_dwordx4 v[178:179], v[204:207], off offset:256
	v_lshl_add_u64 v[178:179], v[178:179], 0, s[26:27]
	s_waitcnt vmcnt(15)
	v_lshlrev_b32_e32 v196, 16, v208
	v_and_b32_e32 v197, 0xffff0000, v208
	v_lshlrev_b32_e32 v228, 16, v209
	v_and_b32_e32 v229, 0xffff0000, v209
	v_lshlrev_b32_e32 v208, 16, v210
	v_and_b32_e32 v209, 0xffff0000, v210
	v_lshlrev_b32_e32 v210, 16, v211
	v_and_b32_e32 v211, 0xffff0000, v211
	v_pk_mul_f32 v[78:79], v[78:79], v[196:197]
	v_pk_mul_f32 v[80:81], v[80:81], v[228:229]
	v_pk_mul_f32 v[74:75], v[74:75], v[208:209]
	v_pk_mul_f32 v[76:77], v[76:77], v[210:211]
	v_cvt_pk_bf16_f32 v208, v78, v79
	v_cvt_pk_bf16_f32 v209, v80, v81
	v_cvt_pk_bf16_f32 v210, v74, v75
	v_cvt_pk_bf16_f32 v211, v76, v77
	global_store_dwordx4 v[178:179], v[208:211], off
	s_waitcnt vmcnt(15)
	v_lshlrev_b32_e32 v196, 16, v212
	v_and_b32_e32 v197, 0xffff0000, v212
	v_lshlrev_b32_e32 v228, 16, v213
	v_and_b32_e32 v229, 0xffff0000, v213
	v_lshlrev_b32_e32 v212, 16, v214
	v_and_b32_e32 v213, 0xffff0000, v214
	v_lshlrev_b32_e32 v214, 16, v215
	v_and_b32_e32 v215, 0xffff0000, v215
	v_pk_mul_f32 v[70:71], v[70:71], v[196:197]
	v_pk_mul_f32 v[72:73], v[72:73], v[228:229]
	v_pk_mul_f32 v[66:67], v[66:67], v[212:213]
	v_pk_mul_f32 v[68:69], v[68:69], v[214:215]
	v_cvt_pk_bf16_f32 v212, v70, v71
	v_cvt_pk_bf16_f32 v213, v72, v73
	v_cvt_pk_bf16_f32 v214, v66, v67
	v_cvt_pk_bf16_f32 v215, v68, v69
	global_store_dwordx4 v[178:179], v[212:215], off offset:256
	s_mov_b64 s[26:27], 0x50000
	v_lshl_add_u64 v[178:179], v[178:179], 0, s[26:27]
	s_mov_b64 s[26:27], 0x10000
	s_waitcnt vmcnt(15)
	v_lshlrev_b32_e32 v196, 16, v216
	v_and_b32_e32 v197, 0xffff0000, v216
	v_lshlrev_b32_e32 v228, 16, v217
	v_and_b32_e32 v229, 0xffff0000, v217
	v_lshlrev_b32_e32 v216, 16, v218
	v_and_b32_e32 v217, 0xffff0000, v218
	v_lshlrev_b32_e32 v218, 16, v219
	v_and_b32_e32 v219, 0xffff0000, v219
	v_pk_mul_f32 v[62:63], v[62:63], v[196:197]
	v_pk_mul_f32 v[64:65], v[64:65], v[228:229]
	v_pk_mul_f32 v[58:59], v[58:59], v[216:217]
	v_pk_mul_f32 v[60:61], v[60:61], v[218:219]
	v_cvt_pk_bf16_f32 v216, v62, v63
	v_cvt_pk_bf16_f32 v217, v64, v65
	v_cvt_pk_bf16_f32 v218, v58, v59
	v_cvt_pk_bf16_f32 v219, v60, v61
	global_store_dwordx4 v[178:179], v[216:219], off
	s_waitcnt vmcnt(15)
	v_lshlrev_b32_e32 v196, 16, v220
	v_and_b32_e32 v197, 0xffff0000, v220
	v_lshlrev_b32_e32 v228, 16, v221
	v_and_b32_e32 v229, 0xffff0000, v221
	v_lshlrev_b32_e32 v220, 16, v222
	v_and_b32_e32 v221, 0xffff0000, v222
	v_lshlrev_b32_e32 v222, 16, v223
	v_and_b32_e32 v223, 0xffff0000, v223
	v_pk_mul_f32 v[54:55], v[54:55], v[196:197]
	v_pk_mul_f32 v[56:57], v[56:57], v[228:229]
	v_pk_mul_f32 v[50:51], v[50:51], v[220:221]
	v_pk_mul_f32 v[52:53], v[52:53], v[222:223]
	v_cvt_pk_bf16_f32 v220, v54, v55
	v_cvt_pk_bf16_f32 v221, v56, v57
	v_cvt_pk_bf16_f32 v222, v50, v51
	v_cvt_pk_bf16_f32 v223, v52, v53
	global_store_dwordx4 v[178:179], v[220:223], off offset:256
	v_lshl_add_u64 v[178:179], v[178:179], 0, s[26:27]
	s_waitcnt vmcnt(15)
	v_lshlrev_b32_e32 v196, 16, v224
	v_and_b32_e32 v197, 0xffff0000, v224
	v_lshlrev_b32_e32 v228, 16, v225
	v_and_b32_e32 v229, 0xffff0000, v225
	v_lshlrev_b32_e32 v224, 16, v226
	v_and_b32_e32 v225, 0xffff0000, v226
	v_lshlrev_b32_e32 v226, 16, v227
	v_and_b32_e32 v227, 0xffff0000, v227
	v_pk_mul_f32 v[46:47], v[46:47], v[196:197]
	v_pk_mul_f32 v[48:49], v[48:49], v[228:229]
	v_pk_mul_f32 v[42:43], v[42:43], v[224:225]
	v_pk_mul_f32 v[44:45], v[44:45], v[226:227]
	v_cvt_pk_bf16_f32 v224, v46, v47
	v_cvt_pk_bf16_f32 v225, v48, v49
	v_cvt_pk_bf16_f32 v226, v42, v43
	v_cvt_pk_bf16_f32 v227, v44, v45
	global_store_dwordx4 v[178:179], v[224:227], off
	s_waitcnt vmcnt(15)
	v_lshlrev_b32_e32 v196, 16, v132
	v_and_b32_e32 v197, 0xffff0000, v132
	v_lshlrev_b32_e32 v228, 16, v133
	v_and_b32_e32 v229, 0xffff0000, v133
	v_lshlrev_b32_e32 v132, 16, v134
	v_and_b32_e32 v133, 0xffff0000, v134
	v_lshlrev_b32_e32 v134, 16, v135
	v_and_b32_e32 v135, 0xffff0000, v135
	v_pk_mul_f32 v[38:39], v[38:39], v[196:197]
	v_pk_mul_f32 v[40:41], v[40:41], v[228:229]
	v_pk_mul_f32 v[34:35], v[34:35], v[132:133]
	v_pk_mul_f32 v[36:37], v[36:37], v[134:135]
	v_cvt_pk_bf16_f32 v132, v38, v39
	v_cvt_pk_bf16_f32 v133, v40, v41
	v_cvt_pk_bf16_f32 v134, v34, v35
	v_cvt_pk_bf16_f32 v135, v36, v37
	global_store_dwordx4 v[178:179], v[132:135], off offset:256
	v_lshl_add_u64 v[178:179], v[178:179], 0, s[26:27]
	s_waitcnt vmcnt(15)
	v_lshlrev_b32_e32 v196, 16, v136
	v_and_b32_e32 v197, 0xffff0000, v136
	v_lshlrev_b32_e32 v228, 16, v137
	v_and_b32_e32 v229, 0xffff0000, v137
	v_lshlrev_b32_e32 v136, 16, v138
	v_and_b32_e32 v137, 0xffff0000, v138
	v_lshlrev_b32_e32 v138, 16, v139
	v_and_b32_e32 v139, 0xffff0000, v139
	v_pk_mul_f32 v[30:31], v[30:31], v[196:197]
	v_pk_mul_f32 v[32:33], v[32:33], v[228:229]
	v_pk_mul_f32 v[26:27], v[26:27], v[136:137]
	v_pk_mul_f32 v[28:29], v[28:29], v[138:139]
	v_cvt_pk_bf16_f32 v136, v30, v31
	v_cvt_pk_bf16_f32 v137, v32, v33
	v_cvt_pk_bf16_f32 v138, v26, v27
	v_cvt_pk_bf16_f32 v139, v28, v29
	global_store_dwordx4 v[178:179], v[136:139], off
	s_waitcnt vmcnt(15)
	v_lshlrev_b32_e32 v196, 16, v140
	v_and_b32_e32 v197, 0xffff0000, v140
	v_lshlrev_b32_e32 v228, 16, v141
	v_and_b32_e32 v229, 0xffff0000, v141
	v_lshlrev_b32_e32 v140, 16, v142
	v_and_b32_e32 v141, 0xffff0000, v142
	v_lshlrev_b32_e32 v142, 16, v143
	v_and_b32_e32 v143, 0xffff0000, v143
	v_pk_mul_f32 v[22:23], v[22:23], v[196:197]
	v_pk_mul_f32 v[24:25], v[24:25], v[228:229]
	v_pk_mul_f32 v[18:19], v[18:19], v[140:141]
	v_pk_mul_f32 v[20:21], v[20:21], v[142:143]
	v_cvt_pk_bf16_f32 v140, v22, v23
	v_cvt_pk_bf16_f32 v141, v24, v25
	v_cvt_pk_bf16_f32 v142, v18, v19
	v_cvt_pk_bf16_f32 v143, v20, v21
	global_store_dwordx4 v[178:179], v[140:143], off offset:256
	v_lshl_add_u64 v[178:179], v[178:179], 0, s[26:27]
	s_waitcnt vmcnt(15)
	v_lshlrev_b32_e32 v196, 16, v168
	v_and_b32_e32 v197, 0xffff0000, v168
	v_lshlrev_b32_e32 v228, 16, v169
	v_and_b32_e32 v229, 0xffff0000, v169
	v_lshlrev_b32_e32 v168, 16, v170
	v_and_b32_e32 v169, 0xffff0000, v170
	v_lshlrev_b32_e32 v170, 16, v171
	v_and_b32_e32 v171, 0xffff0000, v171
	v_pk_mul_f32 v[14:15], v[14:15], v[196:197]
	v_pk_mul_f32 v[16:17], v[16:17], v[228:229]
	v_pk_mul_f32 v[10:11], v[10:11], v[168:169]
	v_pk_mul_f32 v[12:13], v[12:13], v[170:171]
	v_cvt_pk_bf16_f32 v168, v14, v15
	v_cvt_pk_bf16_f32 v169, v16, v17
	v_cvt_pk_bf16_f32 v170, v10, v11
	v_cvt_pk_bf16_f32 v171, v12, v13
	global_store_dwordx4 v[178:179], v[168:171], off
	s_waitcnt vmcnt(15)
	v_lshlrev_b32_e32 v196, 16, v164
	v_and_b32_e32 v197, 0xffff0000, v164
	v_lshlrev_b32_e32 v228, 16, v165
	v_and_b32_e32 v229, 0xffff0000, v165
	v_lshlrev_b32_e32 v164, 16, v166
	v_and_b32_e32 v165, 0xffff0000, v166
	v_lshlrev_b32_e32 v166, 16, v167
	v_and_b32_e32 v167, 0xffff0000, v167
	v_pk_mul_f32 v[6:7], v[6:7], v[196:197]
	v_pk_mul_f32 v[8:9], v[8:9], v[228:229]
	v_pk_mul_f32 v[2:3], v[2:3], v[164:165]
	v_pk_mul_f32 v[4:5], v[4:5], v[166:167]
	v_cvt_pk_bf16_f32 v164, v6, v7
	v_cvt_pk_bf16_f32 v165, v8, v9
	v_cvt_pk_bf16_f32 v166, v2, v3
	v_cvt_pk_bf16_f32 v167, v4, v5
	global_store_dwordx4 v[178:179], v[164:167], off offset:256
	s_andn2_b64 vcc, exec, s[24:25]
	s_mov_b64 s[24:25], -1
	s_cbranch_vccnz .LBB0_1923
	s_andn2_b64 vcc, exec, s[6:7]
	s_cbranch_vccnz .LBB0_1922
	s_barrier
	s_branch .LBB0_1922

.LBB0_2700:
	v_lshl_add_u64 v[52:53], s[90:91], 0, v[46:47]
	v_add_co_u32_e64 v6, s[0:1], s3, v52
	v_lshl_add_u64 v[16:17], s[90:91], 0, v[48:49]
	s_nop 0
	v_addc_co_u32_e64 v7, s[0:1], 0, v53, s[0:1]
	v_add_co_u32_e32 v18, vcc, 0x16000000, v16
	v_add_co_u32_e64 v8, s[0:1], s5, v52
	s_nop 0
	v_addc_co_u32_e32 v19, vcc, 0, v17, vcc
	v_addc_co_u32_e64 v9, s[0:1], 0, v53, s[0:1]
	v_add_co_u32_e64 v24, s[0:1], s13, v52
	v_add_co_u32_e32 v58, vcc, 0x16001000, v16
	v_lshl_add_u64 v[4:5], s[90:91], 0, v[50:51]
	v_addc_co_u32_e64 v25, s[0:1], 0, v53, s[0:1]
	v_addc_co_u32_e32 v59, vcc, 0, v17, vcc
	v_add_co_u32_e64 v26, s[0:1], s14, v4
	v_add_co_u32_e32 v52, vcc, 0x3800000, v52
	s_nop 0
	v_addc_co_u32_e64 v27, s[0:1], 0, v5, s[0:1]
	v_addc_co_u32_e32 v53, vcc, 0, v53, vcc
	global_load_dwordx4 v[0:3], v[36:37], off
	global_load_dword v60, v[8:9], off offset:-4096
	global_load_dword v62, v[6:7], off offset:256
	global_load_dword v66, v[6:7], off offset:512
	global_load_dword v70, v[6:7], off offset:768
	global_load_dword v74, v[6:7], off offset:1024
	global_load_dword v78, v[6:7], off offset:1280
	global_load_dword v82, v[6:7], off offset:1536
	global_load_dword v86, v[6:7], off offset:1792
	global_load_dword v90, v[6:7], off offset:2048
	global_load_dword v122, v[8:9], off
	global_load_dword v126, v[8:9], off offset:256
	global_load_dword v130, v[8:9], off offset:512
	global_load_dword v134, v[8:9], off offset:768
	global_load_dword v138, v[8:9], off offset:1024
	global_load_dword v142, v[8:9], off offset:1280
	global_load_dword v146, v[8:9], off offset:1536
	global_load_dword v150, v[8:9], off offset:1792
	global_load_dword v154, v[8:9], off offset:2048
	global_load_dword v158, v[8:9], off offset:2304
	global_load_dword v162, v[8:9], off offset:2560
	global_load_dword v166, v[8:9], off offset:2816
	global_load_dword v170, v[8:9], off offset:3072
	global_load_dword v174, v[8:9], off offset:3328
	global_load_dword v178, v[8:9], off offset:3584
	global_load_dword v182, v[8:9], off offset:3840
	global_load_dword v94, v[6:7], off offset:2304
	global_load_dword v98, v[6:7], off offset:2560
	global_load_dword v102, v[6:7], off offset:2816
	global_load_dword v106, v[6:7], off offset:3072
	global_load_dword v110, v[6:7], off offset:3328
	global_load_dword v114, v[6:7], off offset:3584
	global_load_dword v118, v[6:7], off offset:3840
	global_load_dword v186, v[24:25], off
	global_load_dword v190, v[24:25], off offset:256
	global_load_dword v228, v[24:25], off offset:512
	global_load_dword v229, v[24:25], off offset:768
	global_load_dword v230, v[24:25], off offset:1024
	global_load_dword v231, v[24:25], off offset:1280
	global_load_dword v232, v[24:25], off offset:1536
	global_load_dword v233, v[24:25], off offset:1792
	global_load_dword v234, v[24:25], off offset:2048
	global_load_dword v235, v[24:25], off offset:2304
	global_load_dword v236, v[24:25], off offset:2560
	global_load_dword v237, v[24:25], off offset:2816
	global_load_dword v238, v[24:25], off offset:3072
	global_load_dword v239, v[24:25], off offset:3328
	global_load_dword v240, v[24:25], off offset:3584
	global_load_dword v241, v[24:25], off offset:3840
	global_load_dword v242, v[26:27], off
	global_load_dword v243, v[26:27], off offset:256
	global_load_dword v244, v[26:27], off offset:512
	global_load_dword v245, v[26:27], off offset:768
	global_load_dword v246, v[26:27], off offset:1024
	global_load_dword v247, v[26:27], off offset:1280
	global_load_dword v248, v[26:27], off offset:1536
	global_load_dword v249, v[26:27], off offset:1792
	global_load_dwordx4 v[20:23], v[18:19], off
	global_load_dwordx4 v[12:15], v[18:19], off offset:1024
	global_load_dwordx4 v[8:11], v[18:19], off offset:2048
	global_load_dwordx4 v[4:7], v[18:19], off offset:3072
	global_load_dwordx4 v[32:35], v[58:59], off
	global_load_dwordx4 v[28:31], v[58:59], off offset:1024
	global_load_dwordx4 v[24:27], v[58:59], off offset:2048
	s_nop 0
	global_load_dwordx4 v[16:19], v[58:59], off offset:3072
	global_load_dword v196, v[52:53], off
	global_load_dword v200, v[52:53], off offset:256
	global_load_dword v204, v[52:53], off offset:512
	global_load_dword v208, v[52:53], off offset:768
	global_load_dword v214, v[52:53], off offset:1024
	global_load_dword v220, v[52:53], off offset:1280
	global_load_dword v224, v[52:53], off offset:1536
	global_load_dword v226, v[52:53], off offset:1792
	global_load_dword v216, v[52:53], off offset:2048
	global_load_dword v218, v[52:53], off offset:2304
	global_load_dword v219, v[52:53], off offset:2560
	global_load_dword v221, v[52:53], off offset:2816
	global_load_dword v222, v[52:53], off offset:3072
	global_load_dword v223, v[52:53], off offset:3328
	global_load_dword v225, v[52:53], off offset:3584
	global_load_dword v227, v[52:53], off offset:3840
	v_mov_b32_e32 v250, 0
	v_mov_b32_e32 v251, 0
	v_lshl_add_u64 v[54:55], s[88:89], 0, v[48:49]
	s_add_i32 s2, s2, s4
	v_lshl_add_u64 v[46:47], v[46:47], 0, s[6:7]
	v_lshl_add_u64 v[48:49], v[48:49], 0, s[8:9]
	v_lshl_add_u64 v[50:51], v[50:51], 0, s[10:11]
	s_cmpk_lt_i32 s2, 0x2000
	s_waitcnt vmcnt(62)
	v_cvt_pk_f32_fp8_e32 v[52:53], v60
	v_cvt_pk_f32_fp8_sdwa v[58:59], v60 src0_sel:WORD_1
	v_cvt_pk_f32_fp8_e32 v[60:61], v62
	v_cvt_pk_f32_fp8_sdwa v[62:63], v62 src0_sel:WORD_1
	v_cvt_pk_f32_fp8_e32 v[64:65], v66
	v_cvt_pk_f32_fp8_sdwa v[66:67], v66 src0_sel:WORD_1
	v_cvt_pk_f32_fp8_e32 v[68:69], v70
	v_cvt_pk_f32_fp8_sdwa v[70:71], v70 src0_sel:WORD_1
	v_cvt_pk_f32_fp8_e32 v[72:73], v74
	v_cvt_pk_f32_fp8_sdwa v[74:75], v74 src0_sel:WORD_1
	v_cvt_pk_f32_fp8_e32 v[88:89], v90
	v_cvt_pk_f32_fp8_sdwa v[90:91], v90 src0_sel:WORD_1
	v_cvt_pk_f32_fp8_e32 v[76:77], v78
	v_cvt_pk_f32_fp8_sdwa v[78:79], v78 src0_sel:WORD_1
	v_cvt_pk_f32_fp8_e32 v[120:121], v122
	v_cvt_pk_f32_fp8_sdwa v[122:123], v122 src0_sel:WORD_1
	v_cvt_pk_f32_fp8_e32 v[124:125], v126
	v_cvt_pk_f32_fp8_sdwa v[126:127], v126 src0_sel:WORD_1
	v_cvt_pk_f32_fp8_e32 v[80:81], v82
	v_cvt_pk_f32_fp8_e32 v[128:129], v130
	v_cvt_pk_f32_fp8_sdwa v[130:131], v130 src0_sel:WORD_1
	v_cvt_pk_f32_fp8_e32 v[152:153], v154
	v_cvt_pk_f32_fp8_sdwa v[154:155], v154 src0_sel:WORD_1
	s_waitcnt vmcnt(61)
	v_cvt_pk_f32_fp8_e32 v[156:157], v158
	v_cvt_pk_f32_fp8_sdwa v[158:159], v158 src0_sel:WORD_1
	s_waitcnt vmcnt(54)
	v_cvt_pk_f32_fp8_e32 v[92:93], v94
	v_cvt_pk_f32_fp8_sdwa v[94:95], v94 src0_sel:WORD_1
	s_waitcnt vmcnt(53)
	v_cvt_pk_f32_fp8_e32 v[96:97], v98
	v_cvt_pk_f32_fp8_sdwa v[98:99], v98 src0_sel:WORD_1
	s_waitcnt vmcnt(52)
	v_cvt_pk_f32_fp8_e32 v[100:101], v102
	v_cvt_pk_f32_fp8_sdwa v[102:103], v102 src0_sel:WORD_1
	v_cvt_pk_f32_fp8_sdwa v[82:83], v82 src0_sel:WORD_1
	s_waitcnt vmcnt(49)
	v_cvt_pk_f32_fp8_e32 v[112:113], v114
	v_cvt_pk_f32_fp8_e32 v[160:161], v162
	v_cvt_pk_f32_fp8_sdwa v[162:163], v162 src0_sel:WORD_1
	s_waitcnt vmcnt(47)
	v_cvt_pk_f32_fp8_e32 v[184:185], v186
	v_cvt_pk_f32_fp8_sdwa v[186:187], v186 src0_sel:WORD_1
	s_waitcnt vmcnt(46)
	v_cvt_pk_f32_fp8_e32 v[188:189], v190
	v_cvt_pk_f32_fp8_sdwa v[190:191], v190 src0_sel:WORD_1
	v_cvt_pk_f32_fp8_e32 v[84:85], v86
	v_cvt_pk_f32_fp8_e32 v[104:105], v106
	v_cvt_pk_f32_fp8_sdwa v[106:107], v106 src0_sel:WORD_1
	v_cvt_pk_f32_fp8_sdwa v[114:115], v114 src0_sel:WORD_1
	v_cvt_pk_f32_fp8_e32 v[132:133], v134
	v_cvt_pk_f32_fp8_sdwa v[134:135], v134 src0_sel:WORD_1
	v_cvt_pk_f32_fp8_e32 v[144:145], v146
	s_waitcnt vmcnt(45)
	v_cvt_pk_f32_fp8_e32 v[192:193], v228
	v_cvt_pk_f32_fp8_sdwa v[86:87], v86 src0_sel:WORD_1
	s_waitcnt vmcnt(15)
	v_cvt_pk_f32_fp8_e32 v[194:195], v196
	v_cvt_pk_f32_fp8_sdwa v[196:197], v196 src0_sel:WORD_1
	s_waitcnt vmcnt(14)
	v_cvt_pk_f32_fp8_e32 v[198:199], v200
	v_cvt_pk_f32_fp8_sdwa v[200:201], v200 src0_sel:WORD_1
	s_waitcnt vmcnt(13)
	v_cvt_pk_f32_fp8_e32 v[202:203], v204
	v_pk_add_f32 v[196:197], v[196:197], 0 op_sel_hi:[1,0]
	v_cvt_pk_f32_fp8_sdwa v[204:205], v204 src0_sel:WORD_1
	v_pk_add_f32 v[200:201], v[200:201], 0 op_sel_hi:[1,0]
	s_waitcnt vmcnt(7)
	v_cvt_pk_f32_fp8_sdwa v[212:213], v216 src0_sel:WORD_1
	v_cvt_pk_f32_fp8_e32 v[216:217], v216
	v_pk_add_f32 v[194:195], v[194:195], 0 op_sel_hi:[1,0]
	v_cvt_pk_f32_fp8_e32 v[206:207], v208
	v_pk_add_f32 v[196:197], v[196:197], v[212:213]
	s_waitcnt vmcnt(6)
	v_cvt_pk_f32_fp8_sdwa v[212:213], v218 src0_sel:WORD_1
	v_cvt_pk_f32_fp8_sdwa v[208:209], v208 src0_sel:WORD_1
	v_pk_add_f32 v[194:195], v[194:195], v[216:217]
	v_cvt_pk_f32_fp8_e32 v[216:217], v218
	v_pk_add_f32 v[200:201], v[200:201], v[212:213]
	s_waitcnt vmcnt(5)
	v_cvt_pk_f32_fp8_sdwa v[212:213], v219 src0_sel:WORD_1
	v_cvt_pk_f32_fp8_e32 v[218:219], v219
	v_pk_add_f32 v[204:205], v[204:205], 0 op_sel_hi:[1,0]
	v_pk_add_f32 v[198:199], v[198:199], 0 op_sel_hi:[1,0]
	v_pk_add_f32 v[204:205], v[204:205], v[212:213]
	s_waitcnt vmcnt(4)
	v_cvt_pk_f32_fp8_sdwa v[212:213], v221 src0_sel:WORD_1
	v_pk_add_f32 v[202:203], v[202:203], 0 op_sel_hi:[1,0]
	v_cvt_pk_f32_fp8_e32 v[210:211], v214
	v_cvt_pk_f32_fp8_sdwa v[214:215], v214 src0_sel:WORD_1
	v_pk_add_f32 v[198:199], v[198:199], v[216:217]
	v_cvt_pk_f32_fp8_e32 v[216:217], v220
	v_pk_add_f32 v[202:203], v[202:203], v[218:219]
	v_cvt_pk_f32_fp8_sdwa v[218:219], v220 src0_sel:WORD_1
	v_cvt_pk_f32_fp8_e32 v[220:221], v221
	v_pk_add_f32 v[208:209], v[208:209], 0 op_sel_hi:[1,0]
	v_pk_add_f32 v[206:207], v[206:207], 0 op_sel_hi:[1,0]
	v_pk_add_f32 v[208:209], v[208:209], v[212:213]
	s_waitcnt vmcnt(3)
	v_cvt_pk_f32_fp8_sdwa v[212:213], v222 src0_sel:WORD_1
	v_pk_add_f32 v[206:207], v[206:207], v[220:221]
	v_cvt_pk_f32_fp8_e32 v[220:221], v222
	v_pk_add_f32 v[214:215], v[214:215], 0 op_sel_hi:[1,0]
	v_pk_add_f32 v[210:211], v[210:211], 0 op_sel_hi:[1,0]
	v_pk_add_f32 v[212:213], v[214:215], v[212:213]
	s_waitcnt vmcnt(2)
	v_cvt_pk_f32_fp8_sdwa v[214:215], v223 src0_sel:WORD_1
	v_cvt_pk_f32_fp8_e32 v[222:223], v223
	v_pk_add_f32 v[210:211], v[210:211], v[220:221]
	v_cvt_pk_f32_fp8_sdwa v[220:221], v224 src0_sel:WORD_1
	v_pk_add_f32 v[218:219], v[218:219], 0 op_sel_hi:[1,0]
	v_pk_add_f32 v[216:217], v[216:217], 0 op_sel_hi:[1,0]
	v_pk_add_f32 v[214:215], v[218:219], v[214:215]
	s_waitcnt vmcnt(1)
	v_cvt_pk_f32_fp8_sdwa v[218:219], v225 src0_sel:WORD_1
	v_pk_add_f32 v[216:217], v[216:217], v[222:223]
	v_cvt_pk_f32_fp8_e32 v[222:223], v224
	v_cvt_pk_f32_fp8_e32 v[224:225], v225
	v_pk_add_f32 v[220:221], v[220:221], 0 op_sel_hi:[1,0]
	v_pk_add_f32 v[52:53], v[194:195], v[52:53]
	v_pk_add_f32 v[218:219], v[220:221], v[218:219]
	v_cvt_pk_f32_fp8_sdwa v[220:221], v226 src0_sel:WORD_1
	v_pk_add_f32 v[222:223], v[222:223], 0 op_sel_hi:[1,0]
	v_pk_add_f32 v[58:59], v[196:197], v[58:59]
	v_pk_add_f32 v[222:223], v[222:223], v[224:225]
	s_waitcnt vmcnt(0)
	v_cvt_pk_f32_fp8_sdwa v[224:225], v227 src0_sel:WORD_1
	v_pk_add_f32 v[220:221], v[220:221], 0 op_sel_hi:[1,0]
	v_pk_add_f32 v[60:61], v[198:199], v[60:61]
	v_pk_add_f32 v[62:63], v[200:201], v[62:63]
	v_pk_add_f32 v[220:221], v[220:221], v[224:225]
	v_cvt_pk_f32_fp8_e32 v[224:225], v226
	v_cvt_pk_f32_fp8_e32 v[226:227], v227
	v_pk_add_f32 v[64:65], v[202:203], v[64:65]
	v_pk_add_f32 v[66:67], v[204:205], v[66:67]
	v_pk_add_f32 v[224:225], v[224:225], 0 op_sel_hi:[1,0]
	v_pk_add_f32 v[70:71], v[208:209], v[70:71]
	v_pk_add_f32 v[224:225], v[224:225], v[226:227]
	v_cvt_pk_f32_fp8_sdwa v[226:227], v228 src0_sel:WORD_1
	v_cvt_pk_f32_fp8_e32 v[208:209], v234
	v_pk_add_f32 v[72:73], v[210:211], v[72:73]
	v_cvt_pk_f32_fp8_sdwa v[210:211], v234 src0_sel:WORD_1
	v_pk_add_f32 v[74:75], v[212:213], v[74:75]
	v_cvt_pk_f32_fp8_e32 v[212:213], v235
	v_cvt_pk_f32_fp8_sdwa v[234:235], v235 src0_sel:WORD_1
	v_pk_add_f32 v[58:59], v[58:59], v[90:91]
	v_pk_add_f32 v[52:53], v[52:53], v[88:89]
	v_pk_add_f32 v[62:63], v[62:63], v[94:95]
	v_pk_add_f32 v[60:61], v[60:61], v[92:93]
	v_cvt_pk_f32_fp8_e32 v[108:109], v110
	v_cvt_pk_f32_fp8_sdwa v[110:111], v110 src0_sel:WORD_1
	v_cvt_pk_f32_fp8_e32 v[116:117], v118
	v_cvt_pk_f32_fp8_e32 v[136:137], v138
	v_cvt_pk_f32_fp8_sdwa v[138:139], v138 src0_sel:WORD_1
	v_cvt_pk_f32_fp8_e32 v[164:165], v166
	v_cvt_pk_f32_fp8_sdwa v[166:167], v166 src0_sel:WORD_1
	v_cvt_pk_f32_fp8_e32 v[176:177], v178
	v_pk_add_f32 v[68:69], v[206:207], v[68:69]
	v_pk_add_f32 v[76:77], v[216:217], v[76:77]
	v_cvt_pk_f32_fp8_e32 v[216:217], v236
	v_pk_add_f32 v[78:79], v[214:215], v[78:79]
	v_cvt_pk_f32_fp8_sdwa v[214:215], v236 src0_sel:WORD_1
	v_cvt_pk_f32_fp8_e32 v[92:93], v242
	v_pk_add_f32 v[66:67], v[66:67], v[98:99]
	v_cvt_pk_f32_fp8_sdwa v[98:99], v242 src0_sel:WORD_1
	v_pk_add_f32 v[64:65], v[64:65], v[96:97]
	v_cvt_pk_f32_fp8_e32 v[96:97], v243
	v_cvt_pk_f32_fp8_sdwa v[242:243], v243 src0_sel:WORD_1
	v_pk_add_f32 v[52:53], v[52:53], v[120:121]
	v_pk_add_f32 v[58:59], v[58:59], v[122:123]
	v_pk_add_f32 v[60:61], v[60:61], v[124:125]
	v_pk_add_f32 v[62:63], v[62:63], v[126:127]
	v_cvt_pk_f32_fp8_sdwa v[118:119], v118 src0_sel:WORD_1
	v_cvt_pk_f32_fp8_e32 v[140:141], v142
	v_cvt_pk_f32_fp8_sdwa v[142:143], v142 src0_sel:WORD_1
	v_cvt_pk_f32_fp8_sdwa v[146:147], v146 src0_sel:WORD_1
	v_cvt_pk_f32_fp8_e32 v[148:149], v150
	v_cvt_pk_f32_fp8_e32 v[168:169], v170
	v_cvt_pk_f32_fp8_sdwa v[170:171], v170 src0_sel:WORD_1
	v_cvt_pk_f32_fp8_e32 v[194:195], v229
	v_cvt_pk_f32_fp8_sdwa v[228:229], v229 src0_sel:WORD_1
	v_cvt_pk_f32_fp8_e32 v[202:203], v232
	v_pk_add_f32 v[80:81], v[222:223], v[80:81]
	v_pk_add_f32 v[70:71], v[70:71], v[102:103]
	v_cvt_pk_f32_fp8_e32 v[102:103], v244
	v_pk_add_f32 v[68:69], v[68:69], v[100:101]
	v_cvt_pk_f32_fp8_sdwa v[100:101], v244 src0_sel:WORD_1
	v_pk_add_f32 v[64:65], v[64:65], v[128:129]
	v_pk_add_f32 v[66:67], v[66:67], v[130:131]
	v_pk_add_f32 v[58:59], v[58:59], v[154:155]
	v_pk_add_f32 v[52:53], v[52:53], v[152:153]
	v_pk_add_f32 v[62:63], v[62:63], v[158:159]
	v_pk_add_f32 v[60:61], v[60:61], v[156:157]
	v_cvt_pk_f32_fp8_e32 v[172:173], v174
	v_cvt_pk_f32_fp8_sdwa v[174:175], v174 src0_sel:WORD_1
	v_cvt_pk_f32_fp8_sdwa v[178:179], v178 src0_sel:WORD_1
	v_cvt_pk_f32_fp8_e32 v[180:181], v182
	v_cvt_pk_f32_fp8_e32 v[196:197], v230
	v_cvt_pk_f32_fp8_sdwa v[198:199], v230 src0_sel:WORD_1
	v_cvt_pk_f32_fp8_e32 v[222:223], v237
	v_cvt_pk_f32_fp8_sdwa v[236:237], v237 src0_sel:WORD_1
	v_pk_add_f32 v[82:83], v[218:219], v[82:83]
	v_cvt_pk_f32_fp8_e32 v[90:91], v240
	v_pk_add_f32 v[80:81], v[80:81], v[112:113]
	v_pk_add_f32 v[66:67], v[66:67], v[162:163]
	v_pk_add_f32 v[64:65], v[64:65], v[160:161]
	v_pk_add_f32 v[52:53], v[52:53], v[184:185]
	v_pk_add_f32 v[58:59], v[58:59], v[186:187]
	v_pk_add_f32 v[60:61], v[60:61], v[188:189]
	v_pk_add_f32 v[62:63], v[62:63], v[190:191]
	v_cvt_pk_f32_fp8_e32 v[200:201], v231
	v_cvt_pk_f32_fp8_sdwa v[230:231], v231 src0_sel:WORD_1
	v_cvt_pk_f32_fp8_sdwa v[204:205], v232 src0_sel:WORD_1
	v_cvt_pk_f32_fp8_e32 v[206:207], v233
	v_cvt_pk_f32_fp8_e32 v[218:219], v238
	v_pk_add_f32 v[84:85], v[224:225], v[84:85]
	v_cvt_pk_f32_fp8_sdwa v[224:225], v238 src0_sel:WORD_1
	v_pk_add_f32 v[74:75], v[74:75], v[106:107]
	v_cvt_pk_f32_fp8_e32 v[106:107], v245
	v_cvt_pk_f32_fp8_sdwa v[244:245], v245 src0_sel:WORD_1
	v_pk_add_f32 v[72:73], v[72:73], v[104:105]
	v_pk_add_f32 v[82:83], v[82:83], v[114:115]
	v_cvt_pk_f32_fp8_e32 v[114:115], v248
	v_pk_add_f32 v[68:69], v[68:69], v[132:133]
	v_pk_add_f32 v[70:71], v[70:71], v[134:135]
	v_pk_add_f32 v[80:81], v[80:81], v[144:145]
	v_pk_add_f32 v[64:65], v[64:65], v[192:193]
	v_pk_add_f32 v[66:67], v[66:67], v[226:227]
	v_pk_add_f32 v[58:59], v[58:59], v[210:211]
	v_pk_add_f32 v[52:53], v[52:53], v[208:209]
	v_pk_add_f32 v[62:63], v[62:63], v[234:235]
	v_pk_add_f32 v[60:61], v[60:61], v[212:213]
	v_cvt_pk_f32_fp8_sdwa v[150:151], v150 src0_sel:WORD_1
	v_pk_add_f32 v[86:87], v[220:221], v[86:87]
	v_cvt_pk_f32_fp8_e32 v[220:221], v239
	v_cvt_pk_f32_fp8_sdwa v[238:239], v239 src0_sel:WORD_1
	v_cvt_pk_f32_fp8_sdwa v[88:89], v240 src0_sel:WORD_1
	v_cvt_pk_f32_fp8_e32 v[94:95], v241
	v_cvt_pk_f32_fp8_e32 v[104:105], v246
	v_pk_add_f32 v[78:79], v[78:79], v[110:111]
	v_cvt_pk_f32_fp8_sdwa v[110:111], v246 src0_sel:WORD_1
	v_pk_add_f32 v[76:77], v[76:77], v[108:109]
	v_pk_add_f32 v[84:85], v[84:85], v[116:117]
	v_pk_add_f32 v[72:73], v[72:73], v[136:137]
	v_pk_add_f32 v[74:75], v[74:75], v[138:139]
	v_pk_add_f32 v[70:71], v[70:71], v[166:167]
	v_pk_add_f32 v[68:69], v[68:69], v[164:165]
	v_pk_add_f32 v[80:81], v[80:81], v[176:177]
	v_pk_add_f32 v[66:67], v[66:67], v[214:215]
	v_pk_add_f32 v[64:65], v[64:65], v[216:217]
	v_pk_add_f32 v[52:53], v[52:53], v[92:93]
	v_pk_add_f32 v[58:59], v[58:59], v[98:99]
	v_pk_add_f32 v[60:61], v[60:61], v[96:97]
	v_pk_add_f32 v[62:63], v[62:63], v[242:243]
	v_cvt_pk_f32_fp8_sdwa v[182:183], v182 src0_sel:WORD_1
	v_cvt_pk_f32_fp8_e32 v[108:109], v247
	v_cvt_pk_f32_fp8_sdwa v[246:247], v247 src0_sel:WORD_1
	v_cvt_pk_f32_fp8_sdwa v[112:113], v248 src0_sel:WORD_1
	v_pk_add_f32 v[86:87], v[86:87], v[118:119]
	v_cvt_pk_f32_fp8_e32 v[118:119], v249
	v_pk_add_f32 v[76:77], v[76:77], v[140:141]
	v_pk_add_f32 v[78:79], v[78:79], v[142:143]
	v_pk_add_f32 v[82:83], v[82:83], v[146:147]
	v_pk_add_f32 v[84:85], v[84:85], v[148:149]
	v_pk_add_f32 v[74:75], v[74:75], v[170:171]
	v_pk_add_f32 v[72:73], v[72:73], v[168:169]
	v_pk_add_f32 v[68:69], v[68:69], v[194:195]
	v_pk_add_f32 v[70:71], v[70:71], v[228:229]
	v_pk_add_f32 v[80:81], v[80:81], v[202:203]
	v_pk_add_f32 v[64:65], v[64:65], v[102:103]
	v_pk_add_f32 v[66:67], v[66:67], v[100:101]
	v_pk_fma_f32 v[22:23], v[58:59], s[12:13], v[22:23] op_sel_hi:[1,0,1]
	v_pk_fma_f32 v[20:21], v[52:53], s[12:13], v[20:21] op_sel_hi:[1,0,1]
	v_pk_fma_f32 v[14:15], v[62:63], s[12:13], v[14:15] op_sel_hi:[1,0,1]
	v_pk_fma_f32 v[12:13], v[60:61], s[12:13], v[12:13] op_sel_hi:[1,0,1]
	v_cvt_pk_f32_fp8_sdwa v[232:233], v233 src0_sel:WORD_1
	v_pk_add_f32 v[78:79], v[78:79], v[174:175]
	v_pk_add_f32 v[76:77], v[76:77], v[172:173]
	v_pk_add_f32 v[82:83], v[82:83], v[178:179]
	v_pk_add_f32 v[84:85], v[84:85], v[180:181]
	v_pk_add_f32 v[72:73], v[72:73], v[196:197]
	v_pk_add_f32 v[74:75], v[74:75], v[198:199]
	v_pk_add_f32 v[70:71], v[70:71], v[236:237]
	v_pk_add_f32 v[68:69], v[68:69], v[222:223]
	v_pk_add_f32 v[80:81], v[80:81], v[90:91]
	v_pk_fma_f32 v[10:11], v[66:67], s[12:13], v[10:11] op_sel_hi:[1,0,1]
	v_pk_fma_f32 v[8:9], v[64:65], s[12:13], v[8:9] op_sel_hi:[1,0,1]
	v_mov_b32_e32 v58, v21
	v_mov_b32_e32 v59, v13
	v_mov_b32_e32 v62, v23
	v_mov_b32_e32 v63, v15
	v_cvt_pk_f32_fp8_sdwa v[240:241], v241 src0_sel:WORD_1
	v_pk_add_f32 v[76:77], v[76:77], v[200:201]
	v_pk_add_f32 v[78:79], v[78:79], v[230:231]
	v_pk_add_f32 v[82:83], v[82:83], v[204:205]
	v_pk_add_f32 v[84:85], v[84:85], v[206:207]
	v_pk_add_f32 v[74:75], v[74:75], v[224:225]
	v_pk_add_f32 v[72:73], v[72:73], v[218:219]
	v_pk_add_f32 v[68:69], v[68:69], v[106:107]
	v_pk_add_f32 v[70:71], v[70:71], v[244:245]
	v_pk_add_f32 v[80:81], v[80:81], v[114:115]
	v_mov_b32_e32 v52, v20
	v_mov_b32_e32 v53, v12
	v_mov_b32_e32 v60, v22
	v_mov_b32_e32 v61, v14
	v_pk_mul_f32 v[64:65], v[10:11], v[10:11]
	v_pk_mul_f32 v[66:67], v[8:9], v[8:9]
	v_pk_mul_f32 v[58:59], v[58:59], v[58:59]
	v_pk_mul_f32 v[62:63], v[62:63], v[62:63]
	v_cvt_pk_f32_fp8_sdwa v[248:249], v249 src0_sel:WORD_1
	v_pk_add_f32 v[86:87], v[86:87], v[150:151]
	v_pk_add_f32 v[78:79], v[78:79], v[238:239]
	v_pk_add_f32 v[76:77], v[76:77], v[220:221]
	v_pk_add_f32 v[82:83], v[82:83], v[88:89]
	v_pk_add_f32 v[84:85], v[84:85], v[94:95]
	v_pk_add_f32 v[72:73], v[72:73], v[104:105]
	v_pk_add_f32 v[74:75], v[74:75], v[110:111]
	v_pk_fma_f32 v[6:7], v[70:71], s[12:13], v[6:7] op_sel_hi:[1,0,1]
	v_pk_fma_f32 v[4:5], v[68:69], s[12:13], v[4:5] op_sel_hi:[1,0,1]
	v_pk_fma_f32 v[24:25], v[80:81], s[12:13], v[24:25] op_sel_hi:[1,0,1]
	v_pk_mov_b32 v[80:81], v[66:67], v[64:65] op_sel:[1,0]
	v_mov_b32_e32 v67, v65
	v_pk_fma_f32 v[52:53], v[52:53], v[52:53], v[58:59]
	v_pk_fma_f32 v[58:59], v[60:61], v[60:61], v[62:63]
	v_pk_add_f32 v[86:87], v[86:87], v[182:183]
	v_pk_add_f32 v[76:77], v[76:77], v[108:109]
	v_pk_add_f32 v[78:79], v[78:79], v[246:247]
	v_pk_add_f32 v[82:83], v[82:83], v[112:113]
	v_pk_add_f32 v[84:85], v[84:85], v[118:119]
	v_pk_fma_f32 v[34:35], v[74:75], s[12:13], v[34:35] op_sel_hi:[1,0,1]
	v_pk_fma_f32 v[32:33], v[72:73], s[12:13], v[32:33] op_sel_hi:[1,0,1]
	v_mul_f32_e32 v68, v5, v5
	v_mul_f32_e32 v70, v7, v7
	v_pk_add_f32 v[60:61], v[80:81], v[66:67]
	v_pk_add_f32 v[52:53], v[52:53], v[58:59]
	v_pk_add_f32 v[86:87], v[86:87], v[232:233]
	v_pk_fma_f32 v[30:31], v[78:79], s[12:13], v[30:31] op_sel_hi:[1,0,1]
	v_pk_fma_f32 v[28:29], v[76:77], s[12:13], v[28:29] op_sel_hi:[1,0,1]
	v_pk_fma_f32 v[26:27], v[82:83], s[12:13], v[26:27] op_sel_hi:[1,0,1]
	v_pk_fma_f32 v[16:17], v[84:85], s[12:13], v[16:17] op_sel_hi:[1,0,1]
	v_mul_f32_e32 v79, v32, v32
	v_mul_f32_e32 v82, v33, v33
	v_mul_f32_e32 v83, v34, v34
	v_mul_f32_e32 v84, v35, v35
	v_pk_fma_f32 v[64:65], v[4:5], v[4:5], v[68:69] op_sel_hi:[1,1,0]
	v_pk_fma_f32 v[68:69], v[6:7], v[6:7], v[70:71] op_sel_hi:[1,1,0]
	v_pk_add_f32 v[58:59], v[60:61], v[60:61] op_sel:[0,1] op_sel_hi:[1,0]
	v_pk_add_f32 v[52:53], v[52:53], v[52:53] op_sel:[0,1] op_sel_hi:[1,0]
	v_pk_add_f32 v[86:87], v[86:87], v[240:241]
	v_pk_mul_f32 v[72:73], v[30:31], v[30:31]
	v_pk_mul_f32 v[74:75], v[28:29], v[28:29]
	v_mov_b32_e32 v65, v83
	v_mov_b32_e32 v69, v84
	v_mov_b32_e32 v59, v82
	v_mov_b32_e32 v53, v79
	v_pk_add_f32 v[86:87], v[86:87], v[248:249]
	v_pk_mov_b32 v[70:71], v[74:75], v[72:73] op_sel:[1,0]
	v_mov_b32_e32 v75, v73
	v_pk_add_f32 v[60:61], v[64:65], v[68:69]
	v_pk_add_f32 v[52:53], v[52:53], v[58:59]
	v_pk_fma_f32 v[18:19], v[86:87], s[12:13], v[18:19] op_sel_hi:[1,0,1]
	global_load_dwordx4 v[100:103], v[36:37], off offset:1024
	global_load_dwordx4 v[104:107], v[36:37], off offset:2048
	global_load_dwordx4 v[108:111], v[36:37], off offset:3072
	global_load_dwordx4 v[112:115], v[38:39], off
	global_load_dwordx4 v[116:119], v[40:41], off
	global_load_dwordx4 v[120:123], v[42:43], off
	global_load_dwordx4 v[124:127], v[44:45], off
	v_mul_f32_e32 v76, v25, v25
	v_mul_f32_e32 v78, v27, v27
	v_pk_add_f32 v[62:63], v[70:71], v[74:75]
	v_pk_add_f32 v[52:53], v[52:53], v[60:61]
	v_mul_f32_e32 v85, v16, v16
	v_mul_f32_e32 v86, v17, v17
	v_mul_f32_e32 v87, v18, v18
	v_mul_f32_e32 v88, v19, v19
	v_pk_fma_f32 v[72:73], v[24:25], v[24:25], v[76:77] op_sel_hi:[1,1,0]
	v_pk_fma_f32 v[76:77], v[26:27], v[26:27], v[78:79] op_sel_hi:[1,1,0]
	v_pk_add_f32 v[62:63], v[62:63], v[62:63] op_sel:[0,1] op_sel_hi:[1,0]
	v_pk_add_f32 v[52:53], v[52:53], v[52:53] op_sel:[0,1] op_sel_hi:[1,0]
	v_mov_b32_e32 v73, v87
	v_mov_b32_e32 v77, v88
	v_mov_b32_e32 v63, v86
	v_mov_b32_e32 v53, v85
	v_pk_add_f32 v[64:65], v[72:73], v[76:77]
	v_pk_add_f32 v[52:53], v[52:53], v[62:63]
	s_nop 0
	v_pk_add_f32 v[52:53], v[52:53], v[64:65]
	s_nop 0
	v_add_f32_e32 v52, v52, v53
	s_nop 1
	v_add_f32_dpp v52, v52, v52 row_shr:1 row_mask:0xf bank_mask:0xf bound_ctrl:1
	s_nop 1
	v_add_f32_dpp v52, v52, v52 row_shr:2 row_mask:0xf bank_mask:0xf bound_ctrl:1
	s_nop 1
	v_add_f32_dpp v52, v52, v52 row_shr:4 row_mask:0xf bank_mask:0xf bound_ctrl:1
	s_nop 1
	v_add_f32_dpp v52, v52, v52 row_shr:8 row_mask:0xf bank_mask:0xf bound_ctrl:1
	s_nop 1
	v_mov_b32_dpp v250, v52 row_bcast:15 row_mask:0xa bank_mask:0xf
	v_add_f32_e32 v52, v52, v250
	s_nop 1
	v_mov_b32_dpp v251, v52 row_bcast:31 row_mask:0xc bank_mask:0xf
	v_add_f32_e32 v52, v52, v251
	s_nop 0
	v_readlane_b32 s0, v52, 63
	s_nop 1
	v_fma_f32 v52, s0, v57, v56
	v_mul_f32_e32 v53, 0x4b800000, v52
	v_cmp_gt_f32_e32 vcc, s15, v52
	s_nop 1
	v_cndmask_b32_e32 v52, v52, v53, vcc
	v_rsq_f32_e32 v52, v52
	s_nop 0
	v_mul_f32_e32 v53, 0x45800000, v52
	v_cndmask_b32_e32 v52, v52, v53, vcc
	v_pk_mul_f32 v[20:21], v[20:21], v[52:53] op_sel_hi:[1,0]
	v_pk_mul_f32 v[22:23], v[22:23], v[52:53] op_sel_hi:[1,0]
	v_pk_mul_f32 v[0:1], v[0:1], v[20:21]
	v_pk_mul_f32 v[2:3], v[2:3], v[22:23]
	global_store_dwordx4 v[54:55], v[0:3], off nt
	v_add_co_u32_e32 v128, vcc, s16, v54
	v_pk_mul_f32 v[12:13], v[12:13], v[52:53] op_sel_hi:[1,0]
	v_pk_mul_f32 v[14:15], v[14:15], v[52:53] op_sel_hi:[1,0]
	v_addc_co_u32_e32 v129, vcc, 0, v55, vcc
	v_pk_mul_f32 v[8:9], v[8:9], v[52:53] op_sel_hi:[1,0]
	v_pk_mul_f32 v[10:11], v[10:11], v[52:53] op_sel_hi:[1,0]
	v_pk_mul_f32 v[4:5], v[4:5], v[52:53] op_sel_hi:[1,0]
	v_pk_mul_f32 v[6:7], v[6:7], v[52:53] op_sel_hi:[1,0]
	v_pk_mul_f32 v[32:33], v[32:33], v[52:53] op_sel_hi:[1,0]
	v_pk_mul_f32 v[34:35], v[34:35], v[52:53] op_sel_hi:[1,0]
	v_pk_mul_f32 v[28:29], v[28:29], v[52:53] op_sel_hi:[1,0]
	v_pk_mul_f32 v[30:31], v[30:31], v[52:53] op_sel_hi:[1,0]
	v_pk_mul_f32 v[24:25], v[24:25], v[52:53] op_sel_hi:[1,0]
	v_pk_mul_f32 v[26:27], v[26:27], v[52:53] op_sel_hi:[1,0]
	v_pk_mul_f32 v[16:17], v[16:17], v[52:53] op_sel_hi:[1,0]
	v_pk_mul_f32 v[18:19], v[18:19], v[52:53] op_sel_hi:[1,0]
	s_waitcnt vmcnt(1)
	v_pk_mul_f32 v[100:101], v[100:101], v[12:13]
	v_pk_mul_f32 v[102:103], v[102:103], v[14:15]
	global_store_dwordx4 v[54:55], v[100:103], off offset:1024 nt
	v_pk_mul_f32 v[104:105], v[104:105], v[8:9]
	v_pk_mul_f32 v[106:107], v[106:107], v[10:11]
	global_store_dwordx4 v[54:55], v[104:107], off offset:2048 nt
	v_pk_mul_f32 v[108:109], v[108:109], v[4:5]
	v_pk_mul_f32 v[110:111], v[110:111], v[6:7]
	global_store_dwordx4 v[54:55], v[108:111], off offset:3072 nt
	v_pk_mul_f32 v[112:113], v[112:113], v[32:33]
	v_pk_mul_f32 v[114:115], v[114:115], v[34:35]
	global_store_dwordx4 v[128:129], v[112:115], off nt
	v_pk_mul_f32 v[116:117], v[116:117], v[28:29]
	v_pk_mul_f32 v[118:119], v[118:119], v[30:31]
	global_store_dwordx4 v[128:129], v[116:119], off offset:1024 nt
	v_pk_mul_f32 v[120:121], v[120:121], v[24:25]
	v_pk_mul_f32 v[122:123], v[122:123], v[26:27]
	global_store_dwordx4 v[128:129], v[120:123], off offset:2048 nt
	v_pk_mul_f32 v[124:125], v[124:125], v[16:17]
	v_pk_mul_f32 v[126:127], v[126:127], v[18:19]
	global_store_dwordx4 v[128:129], v[124:127], off offset:3072 nt
	s_cbranch_scc1 .LBB0_2700
